# local barrier without the atomic return trip (per-wave generation counter); MoBA row max and w_in head-norm sums via permlane swaps
# speedup vs baseline: 1.0323x; 1.0024x over previous
; __device__ __forceinline__ u64_t* ssq_ptr(unsigned char* ws, int v) { return (u64_t*)(ws + CTL_SSQ) + (size_t)v * NTOK; }
; #define OPAQUE_WS() unsigned char* ws = P.ws; asm volatile("" : "+s"(ws)); F.ws = ws; F.tid = fresh_tid(F.wave); asm volatile("" : "+v"(F.tid)); F.lane = F.tid & 63; int c = F.bid; asm volatile("" : "+s"(c))
; #define REP_BEGIN(k) for (int rep_ = 0, nrep_ = ((k) >= PROBE_LO && (k) < PROBE_HI) ? PROBE_N : 0; rep_ <= nrep_; ++rep_) { const bool rerun = PROBE_AFTER ? (rep_ > 0) : (rep_ < nrep_), dry = rerun && PROBE_DRY_;
; __global__ void __launch_bounds__(NTHREADS, 2) mk_fwd(Params P) {
;     ...
; #pragma unroll 1
;     for (int l = 0; l < DEPTH; ++l) {
;         const int pb = 1 + 9 * l;
;         if (PH_EN(0) && IN(pb + 0)) { REP_BEGIN(pb + 0) OPAQUE_WS(); int lq = l; asm volatile("" : "+s"(lq));
;             if (lq == 0 && !rerun) { phase_dense_w13_b(F, P); xcd_barrier(bar); }
;             if (lq > 0) {
;                 { const int gw = F.bid * NWAVES + F.wave, NGW = F.G * NWAVES; const u64_t* ssq = ssq_ptr(ws, 3 * lq); float* rsq = (float*)(ws + WS_RSQA);
;                   quant_pass((const bf16_t*)(ws + WS_XB), ws + AR_XQA, rsq, ssq, gw, NGW, F.lane, dry); }
;                 xcd_barrier(bar);
;             }
;             { Sched2D Sg{(const char*)(ws + AR_XQA), (const char*)(ws + WB_WIN + lq * SZ_WIN), NTOK / 256, OFF_GL / 256, D / 2, G, c, 0, (NTOK / 256) * (OFF_GL / 256)};
;               EpiIn E{ws, P, lq, dry, rerun};
;               pg8::gemm_phase<EpiIn, Sched2D, true, true, true>(F.lds, D / 2, Sg, E, F.wave); }
.LBB0_223:
	s_or_b64 exec, exec, s[30:31]
	v_readlane_b32 s100, v253, 53
	v_readlane_b32 s101, v253, 54
	v_mov_b32_e32 v8, 0
	s_nop 4
	global_load_dwordx4 v[0:3], v8, s[100:101] offset:64 sc1
	global_load_dwordx4 v[4:7], v8, s[100:101] offset:80 sc1
	s_waitcnt vmcnt(0)
	v_bcnt_u32_b32 v8, v0, 0
	v_bcnt_u32_b32 v8, v1, v8
	v_bcnt_u32_b32 v8, v2, v8
	v_bcnt_u32_b32 v8, v3, v8
	v_bcnt_u32_b32 v8, v4, v8
	v_bcnt_u32_b32 v8, v5, v8
	v_bcnt_u32_b32 v8, v6, v8
	v_bcnt_u32_b32 v8, v7, v8
	v_or3_b32 v9, v0, v1, v2
	v_or3_b32 v9, v9, v3, v4
	v_or3_b32 v9, v9, v5, v6
	v_or_b32_e32 v9, v9, v7
	v_bcnt_u32_b32 v9, v9, 0
	v_min_u32_e32 v0, v0, v1
	v_min_u32_e32 v2, v2, v3
	v_min_u32_e32 v4, v4, v5
	v_min_u32_e32 v6, v6, v7
	v_min3_u32 v0, v0, v2, v4
	v_min_u32_e32 v0, v0, v6
	v_readfirstlane_b32 s100, v8
	v_readfirstlane_b32 s101, v0
	s_cmp_eq_u32 s100, 8
	s_cselect_b32 s100, 1, 0
	s_cmp_lg_u32 s101, 0
	s_cselect_b32 s100, s100, 0
	v_readfirstlane_b32 s101, v9
	s_cmp_eq_u32 s101, 8
	s_cselect_b32 s100, s100, 0
	s_mov_b32 s101, 0
	s_cmpk_eq_i32 s78, 0x100
	s_cselect_b32 s100, s100, 0
	s_lshl_b32 s0, s38, 14
	s_add_i32 s0, s0, 0
	s_cmpk_lt_i32 s96, 0xe00
	v_writelane_b32 v254, s0, 28
	s_cselect_b64 s[0:1], -1, 0
	v_writelane_b32 v254, s0, 29
	s_cmpk_lt_i32 s96, 0x700
	s_mov_b32 s93, 0
	v_writelane_b32 v254, s1, 30
	s_cselect_b64 s[0:1], -1, 0
	v_writelane_b32 v254, s0, 31
	s_cmpk_lt_i32 s96, 0x1700
	s_movk_i32 s84, 0x4000
	v_writelane_b32 v254, s1, 32
	s_cselect_b64 s[0:1], -1, 0
	v_writelane_b32 v254, s0, 33
	s_lshl_b32 s2, s78, 5
	s_ashr_i32 s95, s78, 31
	v_writelane_b32 v254, s1, 34
	s_bfe_u32 s0, s33, 0x20006
	v_writelane_b32 v254, s0, 19
	s_lshl_b32 s0, s0, 7
	s_cmpk_lt_i32 s96, 0x4000
	v_writelane_b32 v254, s0, 35
	s_cselect_b64 s[0:1], -1, 0
	s_cmpk_eq_i32 s78, 0x100
	s_cselect_b64 s[4:5], -1, 0
	v_writelane_b32 v254, s4, 10
	v_mov_b32_e32 v113, 0
	v_mov_b32_e32 v248, 1
	v_writelane_b32 v254, s5, 11
	s_add_u32 s4, s86, 0x1000
	s_addc_u32 s5, s87, 0
	v_writelane_b32 v254, s4, 36
	s_cmpk_lt_i32 s96, 0x1c00
	s_mov_b32 s86, s2
	v_writelane_b32 v254, s5, 37
	s_cselect_b64 s[2:3], -1, 0
	v_writelane_b32 v254, s2, 38
	s_cmp_lt_i32 s96, 0xa800
	v_readlane_b32 s4, v253, 0
	v_writelane_b32 v254, s3, 39
	s_cselect_b64 s[2:3], -1, 0
	v_writelane_b32 v254, s2, 40
	s_ashr_i32 s97, s96, 31
	s_ashr_i32 s87, s86, 31
	v_writelane_b32 v254, s3, 41
	s_lshl_b32 s2, s4, 8
	s_lshl_b32 s3, s38, 5
	s_add_i32 s5, s2, s3
	s_lshl_b32 s2, s4, 7
	s_lshl_b32 s3, s38, 4
	s_add_i32 s6, s2, s3
	s_lshl_b32 s2, s4, 4
	s_lshl_b32 s3, s38, 1
	s_add_i32 s7, s2, s3
	s_lshl_b32 s2, s4, 10
	s_lshl_b32 s3, s38, 7
	s_add_i32 s2, s2, s3
	v_writelane_b32 v254, s2, 42
	s_lshl_b32 s2, s4, 11
	s_lshl_b32 s3, s38, 8
	s_add_i32 s2, s2, s3
	v_writelane_b32 v254, s2, 43
	v_writelane_b32 v254, s5, 44
	s_or_b32 s2, s5, 3
	v_writelane_b32 v254, s2, 45
	s_or_b32 s2, s6, 3
	v_writelane_b32 v254, s2, 46
	s_or_b32 s2, s6, 2
	v_writelane_b32 v254, s2, 47
	v_writelane_b32 v254, s6, 48
	s_or_b32 s2, s6, 1
	v_writelane_b32 v254, s2, 49
	s_lshl_b32 s2, s4, 6
	s_lshl_b32 s3, s38, 3
	s_add_i32 s2, s2, s3
	s_add_i32 s2, s2, 0x7ffff200
	v_writelane_b32 v254, s2, 50
	s_lshl_b32 s2, s78, 6
	v_writelane_b32 v254, s2, 51
	s_lshl_b32 s2, s38, 6
	s_add_i32 s2, s36, s2
	v_writelane_b32 v254, s2, 52
	s_sub_i32 s2, 0xa7ff, s96
	s_lshl_b32 s3, s2, 5
	v_writelane_b32 v254, s3, 53
	v_writelane_b32 v254, s2, 54
	s_lshl_b32 s2, s2, 1
	v_writelane_b32 v254, s2, 55
	v_writelane_b32 v254, s7, 56
	s_or_b32 s2, s7, 1
	v_writelane_b32 v254, s2, 57
	s_lshl_b64 s[2:3], s[96:97], 12
	v_writelane_b32 v254, s2, 58
	s_lshl_b32 s75, s78, 8
	s_lshl_b32 s79, s78, 7
	v_writelane_b32 v254, s3, 59
	s_lshl_b64 s[2:3], s[86:87], 12
	v_writelane_b32 v254, s2, 60
	s_lshl_b32 s81, s78, 4
	s_lshl_b32 s82, s78, 10
	s_lshl_b32 s89, s78, 11
	v_writelane_b32 v254, s3, 61
	s_lshl_b64 s[2:3], s[96:97], 11
	s_add_u32 s2, s2, 0x4f00400
	v_writelane_b32 v254, s2, 62
	s_addc_u32 s2, s3, 0
	v_writelane_b32 v254, s2, 63
	s_mov_b32 s2, s96
	v_writelane_b32 v255, s2, 0
	s_xor_b64 s[0:1], s[0:1], -1
	s_movk_i32 s97, 0xe00
	v_writelane_b32 v255, s3, 1
	s_add_i32 s2, s96, s76
	s_ashr_i32 s3, s2, 31
	s_lshl_b64 s[2:3], s[2:3], 12
	v_writelane_b32 v255, s2, 2
	s_movk_i32 s96, 0x5c00
	s_mov_b32 s73, 0x8000
	v_writelane_b32 v255, s3, 3
	s_add_i32 s2, 0, 0x23fa0
	v_writelane_b32 v254, s2, 8
	s_add_i32 s2, 0, 0x23fa4
	v_writelane_b32 v255, s0, 4
	v_writelane_b32 v254, s2, 9
	v_mov_b32_e32 v249, 0x358637bd
	v_writelane_b32 v255, s1, 5
	s_add_i32 s0, 0, 0x11000
	v_writelane_b32 v254, s0, 13
	s_add_i32 s0, 0, 0x1115c
	v_writelane_b32 v254, s0, 12
	s_add_i32 s0, 0, 0x23fc0
	v_writelane_b32 v254, s0, 15
	s_add_i32 s0, 0, 0x23fd0
	v_writelane_b32 v254, s0, 16
	s_add_i32 s0, 0, 0x23fdc
	v_writelane_b32 v255, s0, 6
	s_lshl_b64 s[0:1], s[86:87], 11
	v_writelane_b32 v255, s0, 7
	s_mov_b32 s92, 0xa000
	v_mov_b32_e32 v250, 0x1000
	v_writelane_b32 v255, s1, 8
	s_mov_b32 s0, s76
	v_writelane_b32 v255, s0, 9
	v_mbcnt_hi_u32_b32 v251, -1, v82
	v_mov_b32_e32 v252, 0xf149f2ca
	v_writelane_b32 v255, s1, 10
	s_mov_b32 s0, s86
	v_writelane_b32 v255, s0, 11
	v_mov_b32_e32 v164, 0x43e00000
	s_movk_i32 s85, 0x80
	v_writelane_b32 v255, s1, 12
	v_writelane_b32 v255, s75, 13
	v_writelane_b32 v255, s79, 14
	v_writelane_b32 v255, s81, 15
	v_writelane_b32 v255, s82, 16
	s_mov_b32 s60, 0xc000
	s_mov_b32 s61, 0xe000
	s_mov_b32 s80, 0x41000000
	s_mov_b32 s70, 0xc3e00000
	s_mov_b64 s[34:35], -1
	s_mov_b64 s[66:67], 0x2000
	s_mov_b32 s36, s93
	v_writelane_b32 v254, s95, 14
	v_writelane_b32 v255, s89, 17
	s_waitcnt lgkmcnt(0)
	s_barrier
	s_branch .LBB0_227

; __device__ __forceinline__ float sigmoidf_fast(float x) { return fast_rcp(1.0f + fast_exp2(-x * LOG2E)); }
; __device__ __forceinline__ u32x4 pack8(const f32x4& a, const f32x4& b) { u32x4 w; w.x = pk_bf16(a[0], a[1]); w.y = pk_bf16(a[2], a[3]); w.z = pk_bf16(b[0], b[1]); w.w = pk_bf16(b[2], b[3]); return w; }
;     __device__ __forceinline__ void operator()(const pg8::i32x4 (&acc)[2][2][4][2], const pg8::Unit& u, int wr, int wc, int fr, int fq) const {
;     ...
;             for (int m = 0; m < 4; ++m) {
;                 const int row = u.pm * 256 + ai * 128 + wr * 64 + m * 16 + fr;
;                 const float rs = sq[ai][m];
;                 f32x4 v[2][2];
; #pragma unroll
;                 for (int bj = 0; bj < 2; ++bj)
; #pragma unroll
;                     for (int n = 0; n < 2; ++n)
; #pragma unroll
;                         for (int j = 0; j < 4; ++j) v[bj][n][j] = (float)acc[ai][bj][m][n][j] * (rs * csc[bj][n][j]);
;                 if (kind == 1 || kind == 2) {
;                     float ss = 0.f;
; #pragma unroll
;                     for (int bj = 0; bj < 2; ++bj)
; #pragma unroll
;                         for (int n = 0; n < 2; ++n) ss += (v[bj][n][0] * v[bj][n][0] + v[bj][n][1] * v[bj][n][1]) + (v[bj][n][2] * v[bj][n][2] + v[bj][n][3] * v[bj][n][3]);
;                     ss += __shfl_xor(ss, 16); ss += __shfl_xor(ss, 32);
;                     const float hr = __builtin_amdgcn_rsqf(ss * (1.0f / HD) + EPS);
; #pragma unroll
;                     for (int bj = 0; bj < 2; ++bj)
; #pragma unroll
;                         for (int n = 0; n < 2; ++n) v[bj][n] = v[bj][n] * hr * gv[bj][n];
;                     if (do_kmean) {
; #pragma unroll
;                         for (int bj = 0; bj < 2; ++bj)
; #pragma unroll
;                             for (int n = 0; n < 2; ++n) cs[bj][n] += v[bj][n];
;                     }
;                 } else if (kind == 3) {
; #pragma unroll
;                     for (int bj = 0; bj < 2; ++bj)
; #pragma unroll
;                         for (int n = 0; n < 2; ++n)
; #pragma unroll
;                             for (int j = 0; j < 4; ++j) v[bj][n][j] = sigmoidf_fast(v[bj][n][j] + gv[bj][n][j]);
;                 }
;                 bf16_t* rowp = dst + (size_t)row * ld + col0;
; #pragma unroll
;                 for (int bj = 0; bj < 2; ++bj) if (!dry) *(u32x4*)(rowp + 32 * bj) = pack8(v[bj][0], v[bj][1]);
.LBB0_396:
	v_cvt_f32_i32_e32 v93, v93
	v_cvt_f32_i32_e32 v92, v92
	s_mov_b32 s38, 0x3c010204
	v_cvt_f32_i32_e32 v95, v95
	v_cvt_f32_i32_e32 v94, v94
	s_waitcnt vmcnt(0) lgkmcnt(0)
	v_pk_mul_f32 v[160:161], v[160:161], s[38:39] op_sel_hi:[1,0]
	v_pk_mul_f32 v[162:163], v[162:163], s[38:39] op_sel_hi:[1,0]
	v_pk_mul_f32 v[114:115], v[156:157], s[38:39] op_sel_hi:[1,0]
	v_pk_mul_f32 v[156:157], v[112:113], v[160:161] op_sel_hi:[0,1]
	v_pk_mul_f32 v[208:209], v[156:157], v[92:93]
	v_pk_mul_f32 v[92:93], v[112:113], v[162:163] op_sel_hi:[0,1]
	v_pk_mul_f32 v[206:207], v[92:93], v[94:95]
	v_cvt_f32_i32_e32 v93, v90
	v_cvt_f32_i32_e32 v91, v91
	v_cvt_f32_i32_e32 v90, v89
	v_pk_mul_f32 v[158:159], v[158:159], s[38:39] op_sel_hi:[1,0]
	v_cvt_f32_i32_e32 v85, v85
	v_cvt_f32_i32_e32 v84, v84
	v_mov_b32_e32 v157, v158
	v_mov_b32_e32 v158, v115
	v_cvt_f32_i32_e32 v87, v87
	v_cvt_f32_i32_e32 v86, v86
	v_pk_mul_f32 v[152:153], v[152:153], s[38:39] op_sel_hi:[1,0]
	v_cvt_f32_i32_e32 v92, v88
	v_pk_mul_f32 v[88:89], v[112:113], v[158:159] op_sel_hi:[0,1]
	v_cvt_f32_i32_e32 v81, v81
	v_cvt_f32_i32_e32 v80, v80
	v_pk_mul_f32 v[154:155], v[154:155], s[38:39] op_sel_hi:[1,0]
	v_pk_mul_f32 v[210:211], v[88:89], v[90:91]
	v_pk_mul_f32 v[88:89], v[112:113], v[152:153] op_sel_hi:[0,1]
	v_cvt_f32_i32_e32 v83, v83
	v_cvt_f32_i32_e32 v82, v82
	v_pk_mul_f32 v[148:149], v[148:149], s[38:39] op_sel_hi:[1,0]
	v_pk_mul_f32 v[214:215], v[88:89], v[84:85]
	v_pk_mul_f32 v[84:85], v[112:113], v[154:155] op_sel_hi:[0,1]
	v_pk_mul_f32 v[150:151], v[150:151], s[38:39] op_sel_hi:[1,0]
	s_and_b32 s1, s74, -2
	v_mov_b32_e32 v156, v114
	v_pk_mul_f32 v[212:213], v[84:85], v[86:87]
	v_pk_mul_f32 v[84:85], v[112:113], v[148:149] op_sel_hi:[0,1]
	s_cmp_eq_u32 s1, 2
	v_pk_mul_f32 v[94:95], v[112:113], v[156:157] op_sel_hi:[0,1]
	v_pk_mul_f32 v[218:219], v[84:85], v[80:81]
	v_pk_mul_f32 v[80:81], v[112:113], v[150:151] op_sel_hi:[0,1]
	s_cselect_b64 s[54:55], -1, 0
	v_pk_mul_f32 v[222:223], v[94:95], v[92:93]
	v_pk_mul_f32 v[216:217], v[80:81], v[82:83]
	s_and_b64 vcc, exec, s[58:59]
	s_cbranch_vccz .LBB0_399
	v_mul_f32_e32 v80, v209, v209
	v_mul_f32_e32 v82, v207, v207
	v_pk_mul_f32 v[84:85], v[210:211], v[210:211]
	v_pk_fma_f32 v[80:81], v[208:209], v[208:209], v[80:81] op_sel_hi:[1,1,0]
	v_pk_fma_f32 v[82:83], v[206:207], v[206:207], v[82:83] op_sel_hi:[1,1,0]
	v_pk_fma_f32 v[84:85], v[222:223], v[222:223], v[84:85]
	v_mul_f32_e32 v86, v215, v215
	v_mul_f32_e32 v88, v213, v213
	v_pk_add_f32 v[84:85], v[84:85], v[84:85] op_sel:[0,1] op_sel_hi:[1,0]
	v_pk_fma_f32 v[86:87], v[214:215], v[214:215], v[86:87] op_sel_hi:[1,1,0]
	v_pk_fma_f32 v[88:89], v[212:213], v[212:213], v[88:89] op_sel_hi:[1,1,0]
	v_pk_mul_f32 v[90:91], v[218:219], v[218:219]
	v_pk_mul_f32 v[92:93], v[216:217], v[216:217]
	v_pk_add_f32 v[80:81], v[80:81], v[82:83]
	v_mov_b32_e32 v85, v91
	v_mov_b32_e32 v81, v90
	v_mov_b32_e32 v87, v92
	v_mov_b32_e32 v89, v93
	v_pk_add_f32 v[80:81], v[80:81], v[84:85]
	v_pk_add_f32 v[82:83], v[86:87], v[88:89]
	s_nop 0
	v_pk_add_f32 v[80:81], v[80:81], v[82:83]
	v_and_b32_e32 v82, 64, v251
	v_add_f32_e32 v80, v80, v81
	v_add_u32_e32 v82, 64, v82
	v_mov_b32_e32 v83, v210
	v_mov_b32_e32 v210, v223
	v_mov_b32_e32 v81, v80
	s_nop 1
	v_permlane16_swap_b32_e32 v80, v81
	s_waitcnt lgkmcnt(0)
	v_add_f32_e32 v80, v80, v81
	v_mov_b32_e32 v82, v222
	s_nop 0
	v_mov_b32_e32 v81, v80
	s_nop 1
	v_permlane32_swap_b32_e32 v80, v81
	s_andn2_b64 vcc, exec, s[54:55]
	s_waitcnt lgkmcnt(0)
	v_add_f32_e32 v80, v80, v81
	v_fmamk_f32 v80, v80, 0x3c800000, v249
	v_rsq_f32_e32 v80, v80
	s_nop 0
	v_pk_mul_f32 v[84:85], v[208:209], v[80:81] op_sel_hi:[1,0]
	v_pk_mul_f32 v[82:83], v[82:83], v[80:81] op_sel_hi:[1,0]
	v_pk_mul_f32 v[208:209], v[68:69], v[84:85]
	v_pk_mul_f32 v[84:85], v[210:211], v[80:81] op_sel_hi:[1,0]
	v_pk_mul_f32 v[220:221], v[64:65], v[82:83]
	v_pk_mul_f32 v[82:83], v[214:215], v[80:81] op_sel_hi:[1,0]
	v_pk_mul_f32 v[86:87], v[206:207], v[80:81] op_sel_hi:[1,0]
	v_pk_mul_f32 v[210:211], v[66:67], v[84:85]
	v_pk_mul_f32 v[84:85], v[212:213], v[80:81] op_sel_hi:[1,0]
	v_pk_mul_f32 v[214:215], v[76:77], v[82:83]
	v_pk_mul_f32 v[82:83], v[218:219], v[80:81] op_sel_hi:[1,0]
	v_pk_mul_f32 v[80:81], v[216:217], v[80:81] op_sel_hi:[1,0]
	v_pk_mul_f32 v[206:207], v[70:71], v[86:87]
	v_pk_mul_f32 v[212:213], v[78:79], v[84:85]
	v_pk_mul_f32 v[216:217], v[74:75], v[80:81]
	v_pk_mul_f32 v[218:219], v[72:73], v[82:83]
	s_cbranch_vccnz .LBB0_400
	v_pk_add_f32 v[94:95], v[206:207], 0 op_sel_hi:[1,0]
	v_pk_add_f32 v[92:93], v[208:209], 0 op_sel_hi:[1,0]
	v_pk_add_f32 v[90:91], v[210:211], 0 op_sel_hi:[1,0]
	v_pk_add_f32 v[88:89], v[220:221], 0 op_sel_hi:[1,0]
	v_pk_add_f32 v[86:87], v[212:213], 0 op_sel_hi:[1,0]
	v_pk_add_f32 v[84:85], v[214:215], 0 op_sel_hi:[1,0]
	v_pk_add_f32 v[82:83], v[216:217], 0 op_sel_hi:[1,0]
	v_pk_add_f32 v[80:81], v[218:219], 0 op_sel_hi:[1,0]
	s_branch .LBB0_401

; __device__ __forceinline__ float sigmoidf_fast(float x) { return fast_rcp(1.0f + fast_exp2(-x * LOG2E)); }
; __device__ __forceinline__ u32x4 pack8(const f32x4& a, const f32x4& b) { u32x4 w; w.x = pk_bf16(a[0], a[1]); w.y = pk_bf16(a[2], a[3]); w.z = pk_bf16(b[0], b[1]); w.w = pk_bf16(b[2], b[3]); return w; }
;     __device__ __forceinline__ void operator()(const pg8::i32x4 (&acc)[2][2][4][2], const pg8::Unit& u, int wr, int wc, int fr, int fq) const {
;     ...
;             for (int m = 0; m < 4; ++m) {
;                 const int row = u.pm * 256 + ai * 128 + wr * 64 + m * 16 + fr;
;                 const float rs = sq[ai][m];
;                 f32x4 v[2][2];
; #pragma unroll
;                 for (int bj = 0; bj < 2; ++bj)
; #pragma unroll
;                     for (int n = 0; n < 2; ++n)
; #pragma unroll
;                         for (int j = 0; j < 4; ++j) v[bj][n][j] = (float)acc[ai][bj][m][n][j] * (rs * csc[bj][n][j]);
;                 if (kind == 1 || kind == 2) {
;                     float ss = 0.f;
; #pragma unroll
;                     for (int bj = 0; bj < 2; ++bj)
; #pragma unroll
;                         for (int n = 0; n < 2; ++n) ss += (v[bj][n][0] * v[bj][n][0] + v[bj][n][1] * v[bj][n][1]) + (v[bj][n][2] * v[bj][n][2] + v[bj][n][3] * v[bj][n][3]);
;                     ss += __shfl_xor(ss, 16); ss += __shfl_xor(ss, 32);
;                     const float hr = __builtin_amdgcn_rsqf(ss * (1.0f / HD) + EPS);
; #pragma unroll
;                     for (int bj = 0; bj < 2; ++bj)
; #pragma unroll
;                         for (int n = 0; n < 2; ++n) v[bj][n] = v[bj][n] * hr * gv[bj][n];
;                     if (do_kmean) {
; #pragma unroll
;                         for (int bj = 0; bj < 2; ++bj)
; #pragma unroll
;                             for (int n = 0; n < 2; ++n) cs[bj][n] += v[bj][n];
;                     }
;                 } else if (kind == 3) {
; #pragma unroll
;                     for (int bj = 0; bj < 2; ++bj)
; #pragma unroll
;                         for (int n = 0; n < 2; ++n)
; #pragma unroll
;                             for (int j = 0; j < 4; ++j) v[bj][n][j] = sigmoidf_fast(v[bj][n][j] + gv[bj][n][j]);
;                 }
;                 bf16_t* rowp = dst + (size_t)row * ld + col0;
; #pragma unroll
;                 for (int bj = 0; bj < 2; ++bj) if (!dry) *(u32x4*)(rowp + 32 * bj) = pack8(v[bj][0], v[bj][1]);
.LBB0_401:
	v_ashrrev_i32_e32 v205, 31, v204
	v_lshl_add_u64 v[114:115], v[204:205], 1, s[56:57]
	v_mul_lo_u32 v112, s53, v202
	v_mul_lo_u32 v177, s52, v203
	v_mad_u64_u32 v[202:203], s[56:57], s52, v202, 0
	v_add3_u32 v203, v203, v177, v112
	v_lshl_add_u64 v[222:223], v[202:203], 1, v[114:115]
	v_cvt_pk_bf16_f32 v202, v208, v209
	v_cvt_pk_bf16_f32 v203, v206, v207
	v_cvt_pk_bf16_f32 v204, v220, v221
	v_cvt_pk_bf16_f32 v205, v210, v211
	flat_store_dwordx4 v[222:223], v[202:205]
	v_cvt_f32_i32_e32 v145, v145
	v_cvt_f32_i32_e32 v144, v144
	v_cvt_pk_bf16_f32 v202, v214, v215
	v_cvt_pk_bf16_f32 v203, v212, v213
	v_cvt_pk_bf16_f32 v204, v218, v219
	v_cvt_pk_bf16_f32 v205, v216, v217
	flat_store_dwordx4 v[222:223], v[202:205] offset:64
	v_cvt_f32_i32_e32 v143, v143
	v_cvt_f32_i32_e32 v137, v137
	v_cvt_f32_i32_e32 v203, v147
	v_cvt_f32_i32_e32 v202, v146
	v_pk_mul_f32 v[146:147], v[200:201], v[160:161] op_sel_hi:[0,1]
	v_pk_mul_f32 v[146:147], v[146:147], v[144:145]
	v_pk_mul_f32 v[144:145], v[200:201], v[162:163] op_sel_hi:[0,1]
	v_pk_mul_f32 v[144:145], v[144:145], v[202:203]
	v_cvt_f32_i32_e32 v203, v142
	v_cvt_f32_i32_e32 v202, v140
	v_cvt_f32_i32_e32 v142, v141
	v_pk_mul_f32 v[140:141], v[200:201], v[156:157] op_sel_hi:[0,1]
	v_pk_mul_f32 v[204:205], v[200:201], v[158:159] op_sel_hi:[0,1]
	v_cvt_f32_i32_e32 v136, v136
	v_pk_mul_f32 v[202:203], v[140:141], v[202:203]
	v_pk_mul_f32 v[140:141], v[204:205], v[142:143]
	v_cvt_f32_i32_e32 v143, v139
	v_cvt_f32_i32_e32 v142, v138
	v_cvt_f32_i32_e32 v133, v133
	v_cvt_f32_i32_e32 v132, v132
	v_pk_mul_f32 v[138:139], v[200:201], v[152:153] op_sel_hi:[0,1]
	v_cvt_f32_i32_e32 v205, v135
	v_cvt_f32_i32_e32 v204, v134
	v_pk_mul_f32 v[138:139], v[138:139], v[136:137]
	v_pk_mul_f32 v[136:137], v[200:201], v[154:155] op_sel_hi:[0,1]
	v_pk_mul_f32 v[136:137], v[136:137], v[142:143]
	v_pk_mul_f32 v[142:143], v[200:201], v[148:149] op_sel_hi:[0,1]
	v_pk_mul_f32 v[134:135], v[142:143], v[132:133]
	v_pk_mul_f32 v[132:133], v[200:201], v[150:151] op_sel_hi:[0,1]
	s_and_b64 vcc, exec, s[4:5]
	v_pk_mul_f32 v[132:133], v[132:133], v[204:205]
	s_cbranch_vccnz .LBB0_404
	v_mul_f32_e32 v112, v147, v147
	v_pk_fma_f32 v[142:143], v[146:147], v[146:147], v[112:113] op_sel_hi:[1,1,0]
	v_mul_f32_e32 v112, v145, v145
	v_pk_fma_f32 v[200:201], v[144:145], v[144:145], v[112:113] op_sel_hi:[1,1,0]
	v_pk_mul_f32 v[204:205], v[140:141], v[140:141]
	v_mul_f32_e32 v112, v139, v139
	v_pk_fma_f32 v[204:205], v[202:203], v[202:203], v[204:205]
	v_pk_fma_f32 v[206:207], v[138:139], v[138:139], v[112:113] op_sel_hi:[1,1,0]
	v_mul_f32_e32 v112, v137, v137
	v_pk_add_f32 v[204:205], v[204:205], v[204:205] op_sel:[0,1] op_sel_hi:[1,0]
	v_pk_fma_f32 v[208:209], v[136:137], v[136:137], v[112:113] op_sel_hi:[1,1,0]
	v_pk_mul_f32 v[210:211], v[134:135], v[134:135]
	v_pk_mul_f32 v[212:213], v[132:133], v[132:133]
	v_pk_add_f32 v[142:143], v[142:143], v[200:201]
	v_mov_b32_e32 v205, v211
	v_mov_b32_e32 v143, v210
	v_mov_b32_e32 v207, v212
	v_mov_b32_e32 v209, v213
	v_pk_add_f32 v[142:143], v[142:143], v[204:205]
	v_pk_add_f32 v[200:201], v[206:207], v[208:209]
	s_nop 0
	v_pk_add_f32 v[142:143], v[142:143], v[200:201]
	s_nop 0
	v_add_f32_e32 v112, v142, v143
	v_and_b32_e32 v143, 64, v251
	v_add_u32_e32 v143, 64, v143
	s_nop 1
	v_mov_b32_e32 v142, v112
	s_nop 1
	v_permlane16_swap_b32_e32 v112, v142
	s_waitcnt lgkmcnt(0)
	v_add_f32_e32 v112, v112, v142
	v_mov_b32_e32 v143, v140
	v_mov_b32_e32 v140, v203
	v_mov_b32_e32 v142, v112
	s_nop 1
	v_permlane32_swap_b32_e32 v112, v142
	s_andn2_b64 vcc, exec, s[54:55]
	s_waitcnt lgkmcnt(0)
	v_add_f32_e32 v112, v112, v142
	v_fmamk_f32 v112, v112, 0x3c800000, v249
	v_rsq_f32_e32 v112, v112
	v_mov_b32_e32 v142, v202
	v_pk_mul_f32 v[146:147], v[146:147], v[112:113] op_sel_hi:[1,0]
	v_pk_mul_f32 v[144:145], v[144:145], v[112:113] op_sel_hi:[1,0]
	v_pk_mul_f32 v[142:143], v[142:143], v[112:113] op_sel_hi:[1,0]
	v_pk_mul_f32 v[140:141], v[140:141], v[112:113] op_sel_hi:[1,0]
	v_pk_mul_f32 v[138:139], v[138:139], v[112:113] op_sel_hi:[1,0]
	v_pk_mul_f32 v[136:137], v[136:137], v[112:113] op_sel_hi:[1,0]
	v_pk_mul_f32 v[134:135], v[134:135], v[112:113] op_sel_hi:[1,0]
	v_pk_mul_f32 v[132:133], v[132:133], v[112:113] op_sel_hi:[1,0]
	v_pk_mul_f32 v[144:145], v[70:71], v[144:145]
	v_pk_mul_f32 v[146:147], v[68:69], v[146:147]
	v_pk_mul_f32 v[140:141], v[66:67], v[140:141]
	v_pk_mul_f32 v[142:143], v[64:65], v[142:143]
	v_pk_mul_f32 v[136:137], v[78:79], v[136:137]
	v_pk_mul_f32 v[138:139], v[76:77], v[138:139]
	v_pk_mul_f32 v[132:133], v[74:75], v[132:133]
	v_pk_mul_f32 v[134:135], v[72:73], v[134:135]
	s_cbranch_vccnz .LBB0_405
	v_pk_add_f32 v[94:95], v[94:95], v[144:145]
	v_pk_add_f32 v[92:93], v[92:93], v[146:147]
	v_pk_add_f32 v[90:91], v[90:91], v[140:141]
	v_pk_add_f32 v[88:89], v[88:89], v[142:143]
	v_pk_add_f32 v[86:87], v[86:87], v[136:137]
	v_pk_add_f32 v[84:85], v[84:85], v[138:139]
	v_pk_add_f32 v[82:83], v[82:83], v[132:133]
	v_pk_add_f32 v[80:81], v[80:81], v[134:135]
	s_branch .LBB0_405

; __device__ __forceinline__ float sigmoidf_fast(float x) { return fast_rcp(1.0f + fast_exp2(-x * LOG2E)); }
; __device__ __forceinline__ u32x4 pack8(const f32x4& a, const f32x4& b) { u32x4 w; w.x = pk_bf16(a[0], a[1]); w.y = pk_bf16(a[2], a[3]); w.z = pk_bf16(b[0], b[1]); w.w = pk_bf16(b[2], b[3]); return w; }
;     __device__ __forceinline__ void operator()(const pg8::i32x4 (&acc)[2][2][4][2], const pg8::Unit& u, int wr, int wc, int fr, int fq) const {
;     ...
;             for (int m = 0; m < 4; ++m) {
;                 const int row = u.pm * 256 + ai * 128 + wr * 64 + m * 16 + fr;
;                 const float rs = sq[ai][m];
;                 f32x4 v[2][2];
; #pragma unroll
;                 for (int bj = 0; bj < 2; ++bj)
; #pragma unroll
;                     for (int n = 0; n < 2; ++n)
; #pragma unroll
;                         for (int j = 0; j < 4; ++j) v[bj][n][j] = (float)acc[ai][bj][m][n][j] * (rs * csc[bj][n][j]);
;                 if (kind == 1 || kind == 2) {
;                     float ss = 0.f;
; #pragma unroll
;                     for (int bj = 0; bj < 2; ++bj)
; #pragma unroll
;                         for (int n = 0; n < 2; ++n) ss += (v[bj][n][0] * v[bj][n][0] + v[bj][n][1] * v[bj][n][1]) + (v[bj][n][2] * v[bj][n][2] + v[bj][n][3] * v[bj][n][3]);
;                     ss += __shfl_xor(ss, 16); ss += __shfl_xor(ss, 32);
;                     const float hr = __builtin_amdgcn_rsqf(ss * (1.0f / HD) + EPS);
; #pragma unroll
;                     for (int bj = 0; bj < 2; ++bj)
; #pragma unroll
;                         for (int n = 0; n < 2; ++n) v[bj][n] = v[bj][n] * hr * gv[bj][n];
;                     if (do_kmean) {
; #pragma unroll
;                         for (int bj = 0; bj < 2; ++bj)
; #pragma unroll
;                             for (int n = 0; n < 2; ++n) cs[bj][n] += v[bj][n];
;                     }
;                 } else if (kind == 3) {
; #pragma unroll
;                     for (int bj = 0; bj < 2; ++bj)
; #pragma unroll
;                         for (int n = 0; n < 2; ++n)
; #pragma unroll
;                             for (int j = 0; j < 4; ++j) v[bj][n][j] = sigmoidf_fast(v[bj][n][j] + gv[bj][n][j]);
;                 }
;                 bf16_t* rowp = dst + (size_t)row * ld + col0;
; #pragma unroll
;                 for (int bj = 0; bj < 2; ++bj) if (!dry) *(u32x4*)(rowp + 32 * bj) = pack8(v[bj][0], v[bj][1]);
.LBB0_405:
	v_cvt_f32_i32_e32 v129, v129
	v_cvt_f32_i32_e32 v128, v128
	v_cvt_pk_bf16_f32 v201, v140, v141
	v_cvt_pk_bf16_f32 v141, v132, v133
	v_cvt_f32_i32_e32 v133, v131
	v_cvt_f32_i32_e32 v132, v130
	v_pk_mul_f32 v[130:131], v[196:197], v[160:161] op_sel_hi:[0,1]
	v_pk_mul_f32 v[130:131], v[130:131], v[128:129]
	v_pk_mul_f32 v[128:129], v[196:197], v[162:163] op_sel_hi:[0,1]
	v_pk_mul_f32 v[128:129], v[128:129], v[132:133]
	v_cvt_f32_i32_e32 v133, v126
	v_cvt_f32_i32_e32 v132, v124
	v_cvt_f32_i32_e32 v127, v127
	v_cvt_f32_i32_e32 v126, v125
	v_cvt_pk_bf16_f32 v140, v134, v135
	v_pk_mul_f32 v[124:125], v[196:197], v[156:157] op_sel_hi:[0,1]
	v_pk_mul_f32 v[134:135], v[196:197], v[158:159] op_sel_hi:[0,1]
	v_cvt_f32_i32_e32 v121, v121
	v_cvt_f32_i32_e32 v120, v120
	v_mul_lo_u32 v112, s53, v198
	v_mul_lo_u32 v177, s52, v199
	v_mad_u64_u32 v[198:199], s[56:57], s52, v198, 0
	v_pk_mul_f32 v[132:133], v[124:125], v[132:133]
	v_pk_mul_f32 v[124:125], v[134:135], v[126:127]
	v_cvt_f32_i32_e32 v127, v123
	v_cvt_f32_i32_e32 v126, v122
	v_add3_u32 v199, v199, v177, v112
	v_cvt_f32_i32_e32 v117, v117
	v_cvt_f32_i32_e32 v116, v116
	v_lshl_add_u64 v[202:203], v[198:199], 1, v[114:115]
	v_cvt_pk_bf16_f32 v198, v146, v147
	v_cvt_pk_bf16_f32 v199, v144, v145
	v_cvt_pk_bf16_f32 v200, v142, v143
	v_cvt_pk_bf16_f32 v138, v138, v139
	v_cvt_pk_bf16_f32 v139, v136, v137
	v_pk_mul_f32 v[122:123], v[196:197], v[152:153] op_sel_hi:[0,1]
	v_cvt_f32_i32_e32 v135, v119
	v_cvt_f32_i32_e32 v134, v118
	flat_store_dwordx4 v[202:203], v[198:201]
	flat_store_dwordx4 v[202:203], v[138:141] offset:64
	v_pk_mul_f32 v[122:123], v[122:123], v[120:121]
	v_pk_mul_f32 v[120:121], v[196:197], v[154:155] op_sel_hi:[0,1]
	v_pk_mul_f32 v[120:121], v[120:121], v[126:127]
	v_pk_mul_f32 v[126:127], v[196:197], v[148:149] op_sel_hi:[0,1]
	v_pk_mul_f32 v[118:119], v[126:127], v[116:117]
	v_pk_mul_f32 v[116:117], v[196:197], v[150:151] op_sel_hi:[0,1]
	s_and_b64 vcc, exec, s[4:5]
	v_pk_mul_f32 v[116:117], v[116:117], v[134:135]
	s_cbranch_vccnz .LBB0_408
	v_mul_f32_e32 v112, v131, v131
	v_pk_fma_f32 v[126:127], v[130:131], v[130:131], v[112:113] op_sel_hi:[1,1,0]
	v_mul_f32_e32 v112, v129, v129
	v_pk_fma_f32 v[134:135], v[128:129], v[128:129], v[112:113] op_sel_hi:[1,1,0]
	v_pk_mul_f32 v[136:137], v[124:125], v[124:125]
	v_mul_f32_e32 v112, v123, v123
	v_pk_fma_f32 v[136:137], v[132:133], v[132:133], v[136:137]
	v_pk_fma_f32 v[138:139], v[122:123], v[122:123], v[112:113] op_sel_hi:[1,1,0]
	v_mul_f32_e32 v112, v121, v121
	v_pk_add_f32 v[136:137], v[136:137], v[136:137] op_sel:[0,1] op_sel_hi:[1,0]
	v_pk_fma_f32 v[140:141], v[120:121], v[120:121], v[112:113] op_sel_hi:[1,1,0]
	v_pk_mul_f32 v[142:143], v[118:119], v[118:119]
	v_pk_mul_f32 v[144:145], v[116:117], v[116:117]
	v_pk_add_f32 v[126:127], v[126:127], v[134:135]
	v_mov_b32_e32 v137, v143
	v_mov_b32_e32 v127, v142
	v_mov_b32_e32 v139, v144
	v_mov_b32_e32 v141, v145
	v_pk_add_f32 v[126:127], v[126:127], v[136:137]
	v_pk_add_f32 v[134:135], v[138:139], v[140:141]
	s_nop 0
	v_pk_add_f32 v[126:127], v[126:127], v[134:135]
	s_nop 0
	v_add_f32_e32 v112, v126, v127
	v_and_b32_e32 v127, 64, v251
	v_add_u32_e32 v127, 64, v127
	s_nop 1
	v_mov_b32_e32 v126, v112
	s_nop 1
	v_permlane16_swap_b32_e32 v112, v126
	s_waitcnt lgkmcnt(0)
	v_add_f32_e32 v112, v112, v126
	v_mov_b32_e32 v127, v124
	v_mov_b32_e32 v124, v133
	v_mov_b32_e32 v126, v112
	s_nop 1
	v_permlane32_swap_b32_e32 v112, v126
	s_andn2_b64 vcc, exec, s[54:55]
	s_waitcnt lgkmcnt(0)
	v_add_f32_e32 v112, v112, v126
	v_fmamk_f32 v112, v112, 0x3c800000, v249
	v_rsq_f32_e32 v112, v112
	v_mov_b32_e32 v126, v132
	v_pk_mul_f32 v[130:131], v[130:131], v[112:113] op_sel_hi:[1,0]
	v_pk_mul_f32 v[128:129], v[128:129], v[112:113] op_sel_hi:[1,0]
	v_pk_mul_f32 v[126:127], v[126:127], v[112:113] op_sel_hi:[1,0]
	v_pk_mul_f32 v[124:125], v[124:125], v[112:113] op_sel_hi:[1,0]
	v_pk_mul_f32 v[122:123], v[122:123], v[112:113] op_sel_hi:[1,0]
	v_pk_mul_f32 v[120:121], v[120:121], v[112:113] op_sel_hi:[1,0]
	v_pk_mul_f32 v[118:119], v[118:119], v[112:113] op_sel_hi:[1,0]
	v_pk_mul_f32 v[116:117], v[116:117], v[112:113] op_sel_hi:[1,0]
	v_pk_mul_f32 v[128:129], v[70:71], v[128:129]
	v_pk_mul_f32 v[130:131], v[68:69], v[130:131]
	v_pk_mul_f32 v[124:125], v[66:67], v[124:125]
	v_pk_mul_f32 v[126:127], v[64:65], v[126:127]
	v_pk_mul_f32 v[120:121], v[78:79], v[120:121]
	v_pk_mul_f32 v[122:123], v[76:77], v[122:123]
	v_pk_mul_f32 v[116:117], v[74:75], v[116:117]
	v_pk_mul_f32 v[118:119], v[72:73], v[118:119]
	s_cbranch_vccnz .LBB0_409
	v_pk_add_f32 v[94:95], v[94:95], v[128:129]
	v_pk_add_f32 v[92:93], v[92:93], v[130:131]
	v_pk_add_f32 v[90:91], v[90:91], v[124:125]
	v_pk_add_f32 v[88:89], v[88:89], v[126:127]
	v_pk_add_f32 v[86:87], v[86:87], v[120:121]
	v_pk_add_f32 v[84:85], v[84:85], v[122:123]
	v_pk_add_f32 v[82:83], v[82:83], v[116:117]
	v_pk_add_f32 v[80:81], v[80:81], v[118:119]
	s_branch .LBB0_409

; __device__ __forceinline__ float sigmoidf_fast(float x) { return fast_rcp(1.0f + fast_exp2(-x * LOG2E)); }
; __device__ __forceinline__ u32x4 pack8(const f32x4& a, const f32x4& b) { u32x4 w; w.x = pk_bf16(a[0], a[1]); w.y = pk_bf16(a[2], a[3]); w.z = pk_bf16(b[0], b[1]); w.w = pk_bf16(b[2], b[3]); return w; }
;     __device__ __forceinline__ void operator()(const pg8::i32x4 (&acc)[2][2][4][2], const pg8::Unit& u, int wr, int wc, int fr, int fq) const {
;     ...
;             for (int m = 0; m < 4; ++m) {
;                 const int row = u.pm * 256 + ai * 128 + wr * 64 + m * 16 + fr;
;                 const float rs = sq[ai][m];
;                 f32x4 v[2][2];
; #pragma unroll
;                 for (int bj = 0; bj < 2; ++bj)
; #pragma unroll
;                     for (int n = 0; n < 2; ++n)
; #pragma unroll
;                         for (int j = 0; j < 4; ++j) v[bj][n][j] = (float)acc[ai][bj][m][n][j] * (rs * csc[bj][n][j]);
;                 if (kind == 1 || kind == 2) {
;                     float ss = 0.f;
; #pragma unroll
;                     for (int bj = 0; bj < 2; ++bj)
; #pragma unroll
;                         for (int n = 0; n < 2; ++n) ss += (v[bj][n][0] * v[bj][n][0] + v[bj][n][1] * v[bj][n][1]) + (v[bj][n][2] * v[bj][n][2] + v[bj][n][3] * v[bj][n][3]);
;                     ss += __shfl_xor(ss, 16); ss += __shfl_xor(ss, 32);
;                     const float hr = __builtin_amdgcn_rsqf(ss * (1.0f / HD) + EPS);
; #pragma unroll
;                     for (int bj = 0; bj < 2; ++bj)
; #pragma unroll
;                         for (int n = 0; n < 2; ++n) v[bj][n] = v[bj][n] * hr * gv[bj][n];
;                     if (do_kmean) {
; #pragma unroll
;                         for (int bj = 0; bj < 2; ++bj)
; #pragma unroll
;                             for (int n = 0; n < 2; ++n) cs[bj][n] += v[bj][n];
;                     }
;                 } else if (kind == 3) {
; #pragma unroll
;                     for (int bj = 0; bj < 2; ++bj)
; #pragma unroll
;                         for (int n = 0; n < 2; ++n)
; #pragma unroll
;                             for (int j = 0; j < 4; ++j) v[bj][n][j] = sigmoidf_fast(v[bj][n][j] + gv[bj][n][j]);
;                 }
;                 bf16_t* rowp = dst + (size_t)row * ld + col0;
; #pragma unroll
;                 for (int bj = 0; bj < 2; ++bj) if (!dry) *(u32x4*)(rowp + 32 * bj) = pack8(v[bj][0], v[bj][1]);
.LBB0_409:
	v_mul_lo_u32 v112, s53, v194
	v_mul_lo_u32 v134, s52, v195
	v_mad_u64_u32 v[132:133], s[56:57], s52, v194, 0
	v_add3_u32 v133, v133, v134, v112
	v_cvt_f32_i32_e32 v109, v109
	v_cvt_f32_i32_e32 v108, v108
	v_lshl_add_u64 v[134:135], v[132:133], 1, v[114:115]
	v_cvt_pk_bf16_f32 v133, v124, v125
	v_cvt_pk_bf16_f32 v125, v116, v117
	v_cvt_f32_i32_e32 v117, v111
	v_cvt_f32_i32_e32 v116, v110
	v_pk_mul_f32 v[110:111], v[192:193], v[160:161] op_sel_hi:[0,1]
	v_pk_mul_f32 v[110:111], v[110:111], v[108:109]
	v_pk_mul_f32 v[108:109], v[192:193], v[162:163] op_sel_hi:[0,1]
	v_pk_mul_f32 v[108:109], v[108:109], v[116:117]
	v_cvt_f32_i32_e32 v117, v106
	v_cvt_f32_i32_e32 v116, v104
	v_cvt_f32_i32_e32 v107, v107
	v_cvt_f32_i32_e32 v106, v105
	v_cvt_pk_bf16_f32 v124, v118, v119
	v_pk_mul_f32 v[104:105], v[192:193], v[156:157] op_sel_hi:[0,1]
	v_pk_mul_f32 v[118:119], v[192:193], v[158:159] op_sel_hi:[0,1]
	v_cvt_f32_i32_e32 v101, v101
	v_cvt_f32_i32_e32 v100, v100
	v_pk_mul_f32 v[116:117], v[104:105], v[116:117]
	v_pk_mul_f32 v[104:105], v[118:119], v[106:107]
	v_cvt_f32_i32_e32 v107, v103
	v_cvt_f32_i32_e32 v106, v102
	v_cvt_f32_i32_e32 v97, v97
	v_cvt_f32_i32_e32 v96, v96
	v_cvt_pk_bf16_f32 v130, v130, v131
	v_cvt_pk_bf16_f32 v131, v128, v129
	v_cvt_pk_bf16_f32 v132, v126, v127
	v_cvt_pk_bf16_f32 v122, v122, v123
	v_cvt_pk_bf16_f32 v123, v120, v121
	v_pk_mul_f32 v[102:103], v[192:193], v[152:153] op_sel_hi:[0,1]
	v_cvt_f32_i32_e32 v119, v99
	v_cvt_f32_i32_e32 v118, v98
	flat_store_dwordx4 v[134:135], v[130:133]
	flat_store_dwordx4 v[134:135], v[122:125] offset:64
	v_pk_mul_f32 v[102:103], v[102:103], v[100:101]
	v_pk_mul_f32 v[100:101], v[192:193], v[154:155] op_sel_hi:[0,1]
	v_pk_mul_f32 v[100:101], v[100:101], v[106:107]
	v_pk_mul_f32 v[106:107], v[192:193], v[148:149] op_sel_hi:[0,1]
	v_pk_mul_f32 v[98:99], v[106:107], v[96:97]
	v_pk_mul_f32 v[96:97], v[192:193], v[150:151] op_sel_hi:[0,1]
	s_and_b64 vcc, exec, s[4:5]
	v_pk_mul_f32 v[96:97], v[96:97], v[118:119]
	s_cbranch_vccnz .LBB0_412
	v_mul_f32_e32 v112, v109, v109
	v_mul_f32_e32 v106, v111, v111
	v_pk_fma_f32 v[118:119], v[108:109], v[108:109], v[112:113] op_sel_hi:[1,1,0]
	v_pk_mul_f32 v[120:121], v[104:105], v[104:105]
	v_mul_f32_e32 v112, v103, v103
	v_pk_fma_f32 v[106:107], v[110:111], v[110:111], v[106:107] op_sel_hi:[1,1,0]
	v_pk_fma_f32 v[120:121], v[116:117], v[116:117], v[120:121]
	v_pk_fma_f32 v[122:123], v[102:103], v[102:103], v[112:113] op_sel_hi:[1,1,0]
	v_mul_f32_e32 v112, v101, v101
	v_pk_add_f32 v[120:121], v[120:121], v[120:121] op_sel:[0,1] op_sel_hi:[1,0]
	v_pk_fma_f32 v[124:125], v[100:101], v[100:101], v[112:113] op_sel_hi:[1,1,0]
	v_pk_mul_f32 v[126:127], v[98:99], v[98:99]
	v_pk_mul_f32 v[128:129], v[96:97], v[96:97]
	v_pk_add_f32 v[106:107], v[106:107], v[118:119]
	v_mov_b32_e32 v121, v127
	v_mov_b32_e32 v107, v126
	v_mov_b32_e32 v123, v128
	v_mov_b32_e32 v125, v129
	v_pk_add_f32 v[106:107], v[106:107], v[120:121]
	v_pk_add_f32 v[118:119], v[122:123], v[124:125]
	v_and_b32_e32 v112, 64, v251
	v_pk_add_f32 v[106:107], v[106:107], v[118:119]
	v_add_u32_e32 v112, 64, v112
	v_add_f32_e32 v106, v106, v107
	s_nop 1
	v_mov_b32_e32 v107, v106
	s_nop 1
	v_permlane16_swap_b32_e32 v106, v107
	s_waitcnt lgkmcnt(0)
	v_add_f32_e32 v106, v106, v107
	s_nop 1
	v_mov_b32_e32 v107, v106
	s_nop 1
	v_permlane32_swap_b32_e32 v106, v107
	s_andn2_b64 vcc, exec, s[54:55]
	s_waitcnt lgkmcnt(0)
	v_add_f32_e32 v106, v106, v107
	v_fmamk_f32 v106, v106, 0x3c800000, v249
	v_rsq_f32_e32 v112, v106
	v_mov_b32_e32 v106, v116
	v_mov_b32_e32 v107, v104
	v_mov_b32_e32 v104, v117
	v_pk_mul_f32 v[110:111], v[110:111], v[112:113] op_sel_hi:[1,0]
	v_pk_mul_f32 v[108:109], v[108:109], v[112:113] op_sel_hi:[1,0]
	v_pk_mul_f32 v[106:107], v[106:107], v[112:113] op_sel_hi:[1,0]
	v_pk_mul_f32 v[104:105], v[104:105], v[112:113] op_sel_hi:[1,0]
	v_pk_mul_f32 v[102:103], v[102:103], v[112:113] op_sel_hi:[1,0]
	v_pk_mul_f32 v[100:101], v[100:101], v[112:113] op_sel_hi:[1,0]
	v_pk_mul_f32 v[98:99], v[98:99], v[112:113] op_sel_hi:[1,0]
	v_pk_mul_f32 v[96:97], v[96:97], v[112:113] op_sel_hi:[1,0]
	v_pk_mul_f32 v[108:109], v[70:71], v[108:109]
	v_pk_mul_f32 v[110:111], v[68:69], v[110:111]
	v_pk_mul_f32 v[104:105], v[66:67], v[104:105]
	v_pk_mul_f32 v[106:107], v[64:65], v[106:107]
	v_pk_mul_f32 v[100:101], v[78:79], v[100:101]
	v_pk_mul_f32 v[102:103], v[76:77], v[102:103]
	v_pk_mul_f32 v[96:97], v[74:75], v[96:97]
	v_pk_mul_f32 v[98:99], v[72:73], v[98:99]
	s_cbranch_vccnz .LBB0_413
	v_pk_add_f32 v[94:95], v[94:95], v[108:109]
	v_pk_add_f32 v[92:93], v[92:93], v[110:111]
	v_pk_add_f32 v[90:91], v[90:91], v[104:105]
	v_pk_add_f32 v[88:89], v[88:89], v[106:107]
	v_pk_add_f32 v[86:87], v[86:87], v[100:101]
	v_pk_add_f32 v[84:85], v[84:85], v[102:103]
	v_pk_add_f32 v[82:83], v[82:83], v[96:97]
	v_pk_add_f32 v[80:81], v[80:81], v[98:99]
	s_branch .LBB0_413

; __device__ __forceinline__ float sigmoidf_fast(float x) { return fast_rcp(1.0f + fast_exp2(-x * LOG2E)); }
; __device__ __forceinline__ u32x4 pack8(const f32x4& a, const f32x4& b) { u32x4 w; w.x = pk_bf16(a[0], a[1]); w.y = pk_bf16(a[2], a[3]); w.z = pk_bf16(b[0], b[1]); w.w = pk_bf16(b[2], b[3]); return w; }
;     __device__ __forceinline__ void operator()(const pg8::i32x4 (&acc)[2][2][4][2], const pg8::Unit& u, int wr, int wc, int fr, int fq) const {
;     ...
;             for (int m = 0; m < 4; ++m) {
;                 const int row = u.pm * 256 + ai * 128 + wr * 64 + m * 16 + fr;
;                 const float rs = sq[ai][m];
;                 f32x4 v[2][2];
; #pragma unroll
;                 for (int bj = 0; bj < 2; ++bj)
; #pragma unroll
;                     for (int n = 0; n < 2; ++n)
; #pragma unroll
;                         for (int j = 0; j < 4; ++j) v[bj][n][j] = (float)acc[ai][bj][m][n][j] * (rs * csc[bj][n][j]);
;                 if (kind == 1 || kind == 2) {
;                     float ss = 0.f;
; #pragma unroll
;                     for (int bj = 0; bj < 2; ++bj)
; #pragma unroll
;                         for (int n = 0; n < 2; ++n) ss += (v[bj][n][0] * v[bj][n][0] + v[bj][n][1] * v[bj][n][1]) + (v[bj][n][2] * v[bj][n][2] + v[bj][n][3] * v[bj][n][3]);
;                     ss += __shfl_xor(ss, 16); ss += __shfl_xor(ss, 32);
;                     const float hr = __builtin_amdgcn_rsqf(ss * (1.0f / HD) + EPS);
; #pragma unroll
;                     for (int bj = 0; bj < 2; ++bj)
; #pragma unroll
;                         for (int n = 0; n < 2; ++n) v[bj][n] = v[bj][n] * hr * gv[bj][n];
;                     if (do_kmean) {
; #pragma unroll
;                         for (int bj = 0; bj < 2; ++bj)
; #pragma unroll
;                             for (int n = 0; n < 2; ++n) cs[bj][n] += v[bj][n];
;                     }
;                 } else if (kind == 3) {
; #pragma unroll
;                     for (int bj = 0; bj < 2; ++bj)
; #pragma unroll
;                         for (int n = 0; n < 2; ++n)
; #pragma unroll
;                             for (int j = 0; j < 4; ++j) v[bj][n][j] = sigmoidf_fast(v[bj][n][j] + gv[bj][n][j]);
;                 }
;                 bf16_t* rowp = dst + (size_t)row * ld + col0;
; #pragma unroll
;                 for (int bj = 0; bj < 2; ++bj) if (!dry) *(u32x4*)(rowp + 32 * bj) = pack8(v[bj][0], v[bj][1]);
.LBB0_413:
	v_cvt_f32_i32_e32 v61, v61
	v_cvt_f32_i32_e32 v60, v60
	v_cvt_pk_bf16_f32 v119, v104, v105
	v_cvt_pk_bf16_f32 v105, v96, v97
	v_cvt_f32_i32_e32 v97, v63
	v_cvt_f32_i32_e32 v96, v62
	v_pk_mul_f32 v[62:63], v[188:189], v[160:161] op_sel_hi:[0,1]
	v_pk_mul_f32 v[62:63], v[62:63], v[60:61]
	v_pk_mul_f32 v[60:61], v[188:189], v[162:163] op_sel_hi:[0,1]
	v_pk_mul_f32 v[60:61], v[60:61], v[96:97]
	v_cvt_f32_i32_e32 v97, v58
	v_cvt_f32_i32_e32 v96, v56
	v_cvt_f32_i32_e32 v59, v59
	v_cvt_f32_i32_e32 v58, v57
	v_cvt_pk_bf16_f32 v104, v98, v99
	v_pk_mul_f32 v[56:57], v[188:189], v[156:157] op_sel_hi:[0,1]
	v_pk_mul_f32 v[98:99], v[188:189], v[158:159] op_sel_hi:[0,1]
	v_cvt_f32_i32_e32 v53, v53
	v_cvt_f32_i32_e32 v52, v52
	v_mul_lo_u32 v112, s53, v190
	v_mul_lo_u32 v118, s52, v191
	v_mad_u64_u32 v[116:117], s[56:57], s52, v190, 0
	v_pk_mul_f32 v[96:97], v[56:57], v[96:97]
	v_pk_mul_f32 v[56:57], v[98:99], v[58:59]
	v_cvt_f32_i32_e32 v59, v55
	v_cvt_f32_i32_e32 v58, v54
	v_add3_u32 v117, v117, v118, v112
	v_cvt_f32_i32_e32 v49, v49
	v_cvt_f32_i32_e32 v48, v48
	v_lshl_add_u64 v[120:121], v[116:117], 1, v[114:115]
	v_cvt_pk_bf16_f32 v116, v110, v111
	v_cvt_pk_bf16_f32 v117, v108, v109
	v_cvt_pk_bf16_f32 v118, v106, v107
	v_cvt_pk_bf16_f32 v102, v102, v103
	v_cvt_pk_bf16_f32 v103, v100, v101
	v_pk_mul_f32 v[54:55], v[188:189], v[152:153] op_sel_hi:[0,1]
	v_cvt_f32_i32_e32 v99, v51
	v_cvt_f32_i32_e32 v98, v50
	flat_store_dwordx4 v[120:121], v[116:119]
	flat_store_dwordx4 v[120:121], v[102:105] offset:64
	v_pk_mul_f32 v[54:55], v[54:55], v[52:53]
	v_pk_mul_f32 v[52:53], v[188:189], v[154:155] op_sel_hi:[0,1]
	v_pk_mul_f32 v[52:53], v[52:53], v[58:59]
	v_pk_mul_f32 v[58:59], v[188:189], v[148:149] op_sel_hi:[0,1]
	v_pk_mul_f32 v[50:51], v[58:59], v[48:49]
	v_pk_mul_f32 v[48:49], v[188:189], v[150:151] op_sel_hi:[0,1]
	s_and_b64 vcc, exec, s[4:5]
	v_pk_mul_f32 v[48:49], v[48:49], v[98:99]
	s_cbranch_vccnz .LBB0_416
	v_mul_f32_e32 v58, v63, v63
	v_mul_f32_e32 v98, v61, v61
	v_pk_mul_f32 v[100:101], v[56:57], v[56:57]
	v_pk_fma_f32 v[58:59], v[62:63], v[62:63], v[58:59] op_sel_hi:[1,1,0]
	v_pk_fma_f32 v[98:99], v[60:61], v[60:61], v[98:99] op_sel_hi:[1,1,0]
	v_pk_fma_f32 v[100:101], v[96:97], v[96:97], v[100:101]
	v_mul_f32_e32 v102, v55, v55
	v_mul_f32_e32 v104, v53, v53
	v_pk_add_f32 v[100:101], v[100:101], v[100:101] op_sel:[0,1] op_sel_hi:[1,0]
	v_pk_fma_f32 v[102:103], v[54:55], v[54:55], v[102:103] op_sel_hi:[1,1,0]
	v_pk_fma_f32 v[104:105], v[52:53], v[52:53], v[104:105] op_sel_hi:[1,1,0]
	v_pk_mul_f32 v[106:107], v[50:51], v[50:51]
	v_pk_mul_f32 v[108:109], v[48:49], v[48:49]
	v_pk_add_f32 v[58:59], v[58:59], v[98:99]
	v_mov_b32_e32 v101, v107
	v_mov_b32_e32 v59, v106
	v_mov_b32_e32 v103, v108
	v_mov_b32_e32 v105, v109
	v_pk_add_f32 v[58:59], v[58:59], v[100:101]
	v_pk_add_f32 v[98:99], v[102:103], v[104:105]
	s_nop 0
	v_pk_add_f32 v[58:59], v[58:59], v[98:99]
	v_and_b32_e32 v98, 64, v251
	v_add_f32_e32 v58, v58, v59
	v_add_u32_e32 v98, 64, v98
	s_nop 1
	v_mov_b32_e32 v59, v58
	s_nop 1
	v_permlane16_swap_b32_e32 v58, v59
	s_waitcnt lgkmcnt(0)
	v_add_f32_e32 v58, v58, v59
	s_nop 1
	v_mov_b32_e32 v59, v58
	s_nop 1
	v_permlane32_swap_b32_e32 v58, v59
	s_andn2_b64 vcc, exec, s[54:55]
	s_waitcnt lgkmcnt(0)
	v_add_f32_e32 v58, v58, v59
	v_fmamk_f32 v58, v58, 0x3c800000, v249
	v_rsq_f32_e32 v98, v58
	v_mov_b32_e32 v58, v96
	v_mov_b32_e32 v59, v56
	v_mov_b32_e32 v56, v97
	v_pk_mul_f32 v[62:63], v[62:63], v[98:99] op_sel_hi:[1,0]
	v_pk_mul_f32 v[60:61], v[60:61], v[98:99] op_sel_hi:[1,0]
	v_pk_mul_f32 v[58:59], v[58:59], v[98:99] op_sel_hi:[1,0]
	v_pk_mul_f32 v[56:57], v[56:57], v[98:99] op_sel_hi:[1,0]
	v_pk_mul_f32 v[54:55], v[54:55], v[98:99] op_sel_hi:[1,0]
	v_pk_mul_f32 v[52:53], v[52:53], v[98:99] op_sel_hi:[1,0]
	v_pk_mul_f32 v[50:51], v[50:51], v[98:99] op_sel_hi:[1,0]
	v_pk_mul_f32 v[48:49], v[48:49], v[98:99] op_sel_hi:[1,0]
	v_pk_mul_f32 v[60:61], v[70:71], v[60:61]
	v_pk_mul_f32 v[62:63], v[68:69], v[62:63]
	v_pk_mul_f32 v[56:57], v[66:67], v[56:57]
	v_pk_mul_f32 v[58:59], v[64:65], v[58:59]
	v_pk_mul_f32 v[52:53], v[78:79], v[52:53]
	v_pk_mul_f32 v[54:55], v[76:77], v[54:55]
	v_pk_mul_f32 v[48:49], v[74:75], v[48:49]
	v_pk_mul_f32 v[50:51], v[72:73], v[50:51]
	s_cbranch_vccnz .LBB0_417
	v_pk_add_f32 v[94:95], v[94:95], v[60:61]
	v_pk_add_f32 v[92:93], v[92:93], v[62:63]
	v_pk_add_f32 v[90:91], v[90:91], v[56:57]
	v_pk_add_f32 v[88:89], v[88:89], v[58:59]
	v_pk_add_f32 v[86:87], v[86:87], v[52:53]
	v_pk_add_f32 v[84:85], v[84:85], v[54:55]
	v_pk_add_f32 v[82:83], v[82:83], v[48:49]
	v_pk_add_f32 v[80:81], v[80:81], v[50:51]
	s_branch .LBB0_417

; __device__ __forceinline__ float sigmoidf_fast(float x) { return fast_rcp(1.0f + fast_exp2(-x * LOG2E)); }
; __device__ __forceinline__ u32x4 pack8(const f32x4& a, const f32x4& b) { u32x4 w; w.x = pk_bf16(a[0], a[1]); w.y = pk_bf16(a[2], a[3]); w.z = pk_bf16(b[0], b[1]); w.w = pk_bf16(b[2], b[3]); return w; }
;     __device__ __forceinline__ void operator()(const pg8::i32x4 (&acc)[2][2][4][2], const pg8::Unit& u, int wr, int wc, int fr, int fq) const {
;     ...
;             for (int m = 0; m < 4; ++m) {
;                 const int row = u.pm * 256 + ai * 128 + wr * 64 + m * 16 + fr;
;                 const float rs = sq[ai][m];
;                 f32x4 v[2][2];
; #pragma unroll
;                 for (int bj = 0; bj < 2; ++bj)
; #pragma unroll
;                     for (int n = 0; n < 2; ++n)
; #pragma unroll
;                         for (int j = 0; j < 4; ++j) v[bj][n][j] = (float)acc[ai][bj][m][n][j] * (rs * csc[bj][n][j]);
;                 if (kind == 1 || kind == 2) {
;                     float ss = 0.f;
; #pragma unroll
;                     for (int bj = 0; bj < 2; ++bj)
; #pragma unroll
;                         for (int n = 0; n < 2; ++n) ss += (v[bj][n][0] * v[bj][n][0] + v[bj][n][1] * v[bj][n][1]) + (v[bj][n][2] * v[bj][n][2] + v[bj][n][3] * v[bj][n][3]);
;                     ss += __shfl_xor(ss, 16); ss += __shfl_xor(ss, 32);
;                     const float hr = __builtin_amdgcn_rsqf(ss * (1.0f / HD) + EPS);
; #pragma unroll
;                     for (int bj = 0; bj < 2; ++bj)
; #pragma unroll
;                         for (int n = 0; n < 2; ++n) v[bj][n] = v[bj][n] * hr * gv[bj][n];
;                     if (do_kmean) {
; #pragma unroll
;                         for (int bj = 0; bj < 2; ++bj)
; #pragma unroll
;                             for (int n = 0; n < 2; ++n) cs[bj][n] += v[bj][n];
;                     }
;                 } else if (kind == 3) {
; #pragma unroll
;                     for (int bj = 0; bj < 2; ++bj)
; #pragma unroll
;                         for (int n = 0; n < 2; ++n)
; #pragma unroll
;                             for (int j = 0; j < 4; ++j) v[bj][n][j] = sigmoidf_fast(v[bj][n][j] + gv[bj][n][j]);
;                 }
;                 bf16_t* rowp = dst + (size_t)row * ld + col0;
; #pragma unroll
;                 for (int bj = 0; bj < 2; ++bj) if (!dry) *(u32x4*)(rowp + 32 * bj) = pack8(v[bj][0], v[bj][1]);
.LBB0_417:
	v_mul_lo_u32 v98, s53, v186
	v_mul_lo_u32 v99, s52, v187
	v_mad_u64_u32 v[96:97], s[56:57], s52, v186, 0
	v_cvt_f32_i32_e32 v45, v45
	v_cvt_f32_i32_e32 v44, v44
	v_add3_u32 v97, v97, v99, v98
	v_cvt_pk_bf16_f32 v99, v56, v57
	v_cvt_pk_bf16_f32 v57, v48, v49
	v_cvt_f32_i32_e32 v49, v47
	v_cvt_f32_i32_e32 v48, v46
	v_pk_mul_f32 v[46:47], v[184:185], v[160:161] op_sel_hi:[0,1]
	v_pk_mul_f32 v[46:47], v[46:47], v[44:45]
	v_pk_mul_f32 v[44:45], v[184:185], v[162:163] op_sel_hi:[0,1]
	v_pk_mul_f32 v[44:45], v[44:45], v[48:49]
	v_cvt_f32_i32_e32 v49, v42
	v_cvt_f32_i32_e32 v48, v40
	v_cvt_f32_i32_e32 v43, v43
	v_cvt_f32_i32_e32 v42, v41
	v_cvt_pk_bf16_f32 v56, v50, v51
	v_pk_mul_f32 v[40:41], v[184:185], v[156:157] op_sel_hi:[0,1]
	v_pk_mul_f32 v[50:51], v[184:185], v[158:159] op_sel_hi:[0,1]
	v_cvt_f32_i32_e32 v37, v37
	v_cvt_f32_i32_e32 v36, v36
	v_pk_mul_f32 v[48:49], v[40:41], v[48:49]
	v_pk_mul_f32 v[40:41], v[50:51], v[42:43]
	v_cvt_f32_i32_e32 v43, v39
	v_cvt_f32_i32_e32 v42, v38
	v_cvt_f32_i32_e32 v33, v33
	v_cvt_f32_i32_e32 v32, v32
	v_lshl_add_u64 v[100:101], v[96:97], 1, v[114:115]
	v_cvt_pk_bf16_f32 v96, v62, v63
	v_cvt_pk_bf16_f32 v97, v60, v61
	v_cvt_pk_bf16_f32 v98, v58, v59
	v_cvt_pk_bf16_f32 v54, v54, v55
	v_cvt_pk_bf16_f32 v55, v52, v53
	v_pk_mul_f32 v[38:39], v[184:185], v[152:153] op_sel_hi:[0,1]
	v_cvt_f32_i32_e32 v51, v35
	v_cvt_f32_i32_e32 v50, v34
	flat_store_dwordx4 v[100:101], v[96:99]
	flat_store_dwordx4 v[100:101], v[54:57] offset:64
	v_pk_mul_f32 v[38:39], v[38:39], v[36:37]
	v_pk_mul_f32 v[36:37], v[184:185], v[154:155] op_sel_hi:[0,1]
	v_pk_mul_f32 v[36:37], v[36:37], v[42:43]
	v_pk_mul_f32 v[42:43], v[184:185], v[148:149] op_sel_hi:[0,1]
	v_pk_mul_f32 v[34:35], v[42:43], v[32:33]
	v_pk_mul_f32 v[32:33], v[184:185], v[150:151] op_sel_hi:[0,1]
	s_and_b64 vcc, exec, s[4:5]
	v_pk_mul_f32 v[32:33], v[32:33], v[50:51]
	s_cbranch_vccnz .LBB0_420
	v_mul_f32_e32 v42, v47, v47
	v_mul_f32_e32 v50, v45, v45
	v_pk_mul_f32 v[52:53], v[40:41], v[40:41]
	v_pk_fma_f32 v[42:43], v[46:47], v[46:47], v[42:43] op_sel_hi:[1,1,0]
	v_pk_fma_f32 v[50:51], v[44:45], v[44:45], v[50:51] op_sel_hi:[1,1,0]
	v_pk_fma_f32 v[52:53], v[48:49], v[48:49], v[52:53]
	v_mul_f32_e32 v54, v39, v39
	v_mul_f32_e32 v56, v37, v37
	v_pk_add_f32 v[52:53], v[52:53], v[52:53] op_sel:[0,1] op_sel_hi:[1,0]
	v_pk_fma_f32 v[54:55], v[38:39], v[38:39], v[54:55] op_sel_hi:[1,1,0]
	v_pk_fma_f32 v[56:57], v[36:37], v[36:37], v[56:57] op_sel_hi:[1,1,0]
	v_pk_mul_f32 v[58:59], v[34:35], v[34:35]
	v_pk_mul_f32 v[60:61], v[32:33], v[32:33]
	v_pk_add_f32 v[42:43], v[42:43], v[50:51]
	v_mov_b32_e32 v53, v59
	v_mov_b32_e32 v43, v58
	v_mov_b32_e32 v55, v60
	v_mov_b32_e32 v57, v61
	v_pk_add_f32 v[42:43], v[42:43], v[52:53]
	v_pk_add_f32 v[50:51], v[54:55], v[56:57]
	s_nop 0
	v_pk_add_f32 v[42:43], v[42:43], v[50:51]
	v_and_b32_e32 v50, 64, v251
	v_add_f32_e32 v42, v42, v43
	v_add_u32_e32 v50, 64, v50
	s_nop 1
	v_mov_b32_e32 v43, v42
	s_nop 1
	v_permlane16_swap_b32_e32 v42, v43
	s_waitcnt lgkmcnt(0)
	v_add_f32_e32 v42, v42, v43
	s_nop 1
	v_mov_b32_e32 v43, v42
	s_nop 1
	v_permlane32_swap_b32_e32 v42, v43
	s_andn2_b64 vcc, exec, s[54:55]
	s_waitcnt lgkmcnt(0)
	v_add_f32_e32 v42, v42, v43
	v_fmamk_f32 v42, v42, 0x3c800000, v249
	v_rsq_f32_e32 v50, v42
	v_mov_b32_e32 v42, v48
	v_mov_b32_e32 v43, v40
	v_mov_b32_e32 v40, v49
	v_pk_mul_f32 v[46:47], v[46:47], v[50:51] op_sel_hi:[1,0]
	v_pk_mul_f32 v[44:45], v[44:45], v[50:51] op_sel_hi:[1,0]
	v_pk_mul_f32 v[42:43], v[42:43], v[50:51] op_sel_hi:[1,0]
	v_pk_mul_f32 v[40:41], v[40:41], v[50:51] op_sel_hi:[1,0]
	v_pk_mul_f32 v[38:39], v[38:39], v[50:51] op_sel_hi:[1,0]
	v_pk_mul_f32 v[36:37], v[36:37], v[50:51] op_sel_hi:[1,0]
	v_pk_mul_f32 v[34:35], v[34:35], v[50:51] op_sel_hi:[1,0]
	v_pk_mul_f32 v[32:33], v[32:33], v[50:51] op_sel_hi:[1,0]
	v_pk_mul_f32 v[44:45], v[70:71], v[44:45]
	v_pk_mul_f32 v[46:47], v[68:69], v[46:47]
	v_pk_mul_f32 v[40:41], v[66:67], v[40:41]
	v_pk_mul_f32 v[42:43], v[64:65], v[42:43]
	v_pk_mul_f32 v[36:37], v[78:79], v[36:37]
	v_pk_mul_f32 v[38:39], v[76:77], v[38:39]
	v_pk_mul_f32 v[32:33], v[74:75], v[32:33]
	v_pk_mul_f32 v[34:35], v[72:73], v[34:35]
	s_cbranch_vccnz .LBB0_421
	v_pk_add_f32 v[94:95], v[94:95], v[44:45]
	v_pk_add_f32 v[92:93], v[92:93], v[46:47]
	v_pk_add_f32 v[90:91], v[90:91], v[40:41]
	v_pk_add_f32 v[88:89], v[88:89], v[42:43]
	v_pk_add_f32 v[86:87], v[86:87], v[36:37]
	v_pk_add_f32 v[84:85], v[84:85], v[38:39]
	v_pk_add_f32 v[82:83], v[82:83], v[32:33]
	v_pk_add_f32 v[80:81], v[80:81], v[34:35]
	s_branch .LBB0_421

; __device__ __forceinline__ float sigmoidf_fast(float x) { return fast_rcp(1.0f + fast_exp2(-x * LOG2E)); }
; __device__ __forceinline__ u32x4 pack8(const f32x4& a, const f32x4& b) { u32x4 w; w.x = pk_bf16(a[0], a[1]); w.y = pk_bf16(a[2], a[3]); w.z = pk_bf16(b[0], b[1]); w.w = pk_bf16(b[2], b[3]); return w; }
;     __device__ __forceinline__ void operator()(const pg8::i32x4 (&acc)[2][2][4][2], const pg8::Unit& u, int wr, int wc, int fr, int fq) const {
;     ...
;             for (int m = 0; m < 4; ++m) {
;                 const int row = u.pm * 256 + ai * 128 + wr * 64 + m * 16 + fr;
;                 const float rs = sq[ai][m];
;                 f32x4 v[2][2];
; #pragma unroll
;                 for (int bj = 0; bj < 2; ++bj)
; #pragma unroll
;                     for (int n = 0; n < 2; ++n)
; #pragma unroll
;                         for (int j = 0; j < 4; ++j) v[bj][n][j] = (float)acc[ai][bj][m][n][j] * (rs * csc[bj][n][j]);
;                 if (kind == 1 || kind == 2) {
;                     float ss = 0.f;
; #pragma unroll
;                     for (int bj = 0; bj < 2; ++bj)
; #pragma unroll
;                         for (int n = 0; n < 2; ++n) ss += (v[bj][n][0] * v[bj][n][0] + v[bj][n][1] * v[bj][n][1]) + (v[bj][n][2] * v[bj][n][2] + v[bj][n][3] * v[bj][n][3]);
;                     ss += __shfl_xor(ss, 16); ss += __shfl_xor(ss, 32);
;                     const float hr = __builtin_amdgcn_rsqf(ss * (1.0f / HD) + EPS);
; #pragma unroll
;                     for (int bj = 0; bj < 2; ++bj)
; #pragma unroll
;                         for (int n = 0; n < 2; ++n) v[bj][n] = v[bj][n] * hr * gv[bj][n];
;                     if (do_kmean) {
; #pragma unroll
;                         for (int bj = 0; bj < 2; ++bj)
; #pragma unroll
;                             for (int n = 0; n < 2; ++n) cs[bj][n] += v[bj][n];
;                     }
;                 } else if (kind == 3) {
; #pragma unroll
;                     for (int bj = 0; bj < 2; ++bj)
; #pragma unroll
;                         for (int n = 0; n < 2; ++n)
; #pragma unroll
;                             for (int j = 0; j < 4; ++j) v[bj][n][j] = sigmoidf_fast(v[bj][n][j] + gv[bj][n][j]);
;                 }
;                 bf16_t* rowp = dst + (size_t)row * ld + col0;
; #pragma unroll
;                 for (int bj = 0; bj < 2; ++bj) if (!dry) *(u32x4*)(rowp + 32 * bj) = pack8(v[bj][0], v[bj][1]);
.LBB0_421:
	v_mul_lo_u32 v50, s53, v182
	v_mul_lo_u32 v51, s52, v183
	v_mad_u64_u32 v[48:49], s[56:57], s52, v182, 0
	v_add3_u32 v49, v49, v51, v50
	v_cvt_f32_i32_e32 v29, v29
	v_cvt_f32_i32_e32 v28, v28
	v_lshl_add_u64 v[50:51], v[48:49], 1, v[114:115]
	v_cvt_pk_bf16_f32 v49, v40, v41
	v_cvt_pk_bf16_f32 v41, v32, v33
	v_cvt_f32_i32_e32 v33, v31
	v_cvt_f32_i32_e32 v32, v30
	v_pk_mul_f32 v[30:31], v[180:181], v[160:161] op_sel_hi:[0,1]
	v_pk_mul_f32 v[30:31], v[30:31], v[28:29]
	v_pk_mul_f32 v[28:29], v[180:181], v[162:163] op_sel_hi:[0,1]
	v_pk_mul_f32 v[28:29], v[28:29], v[32:33]
	v_cvt_f32_i32_e32 v33, v26
	v_cvt_f32_i32_e32 v32, v24
	v_cvt_f32_i32_e32 v27, v27
	v_cvt_f32_i32_e32 v26, v25
	v_cvt_pk_bf16_f32 v40, v34, v35
	v_pk_mul_f32 v[24:25], v[180:181], v[156:157] op_sel_hi:[0,1]
	v_pk_mul_f32 v[34:35], v[180:181], v[158:159] op_sel_hi:[0,1]
	v_cvt_f32_i32_e32 v21, v21
	v_cvt_f32_i32_e32 v20, v20
	v_pk_mul_f32 v[32:33], v[24:25], v[32:33]
	v_pk_mul_f32 v[24:25], v[34:35], v[26:27]
	v_cvt_f32_i32_e32 v27, v23
	v_cvt_f32_i32_e32 v26, v22
	v_cvt_f32_i32_e32 v17, v17
	v_cvt_f32_i32_e32 v16, v16
	v_cvt_pk_bf16_f32 v46, v46, v47
	v_cvt_pk_bf16_f32 v47, v44, v45
	v_cvt_pk_bf16_f32 v48, v42, v43
	v_cvt_pk_bf16_f32 v38, v38, v39
	v_cvt_pk_bf16_f32 v39, v36, v37
	v_pk_mul_f32 v[22:23], v[180:181], v[152:153] op_sel_hi:[0,1]
	v_cvt_f32_i32_e32 v35, v19
	v_cvt_f32_i32_e32 v34, v18
	flat_store_dwordx4 v[50:51], v[46:49]
	flat_store_dwordx4 v[50:51], v[38:41] offset:64
	v_pk_mul_f32 v[22:23], v[22:23], v[20:21]
	v_pk_mul_f32 v[20:21], v[180:181], v[154:155] op_sel_hi:[0,1]
	v_pk_mul_f32 v[20:21], v[20:21], v[26:27]
	v_pk_mul_f32 v[26:27], v[180:181], v[148:149] op_sel_hi:[0,1]
	v_pk_mul_f32 v[18:19], v[26:27], v[16:17]
	v_pk_mul_f32 v[16:17], v[180:181], v[150:151] op_sel_hi:[0,1]
	s_and_b64 vcc, exec, s[4:5]
	v_pk_mul_f32 v[16:17], v[16:17], v[34:35]
	s_cbranch_vccnz .LBB0_424
	v_mul_f32_e32 v26, v31, v31
	v_mul_f32_e32 v34, v29, v29
	v_pk_mul_f32 v[36:37], v[24:25], v[24:25]
	v_pk_fma_f32 v[26:27], v[30:31], v[30:31], v[26:27] op_sel_hi:[1,1,0]
	v_pk_fma_f32 v[34:35], v[28:29], v[28:29], v[34:35] op_sel_hi:[1,1,0]
	v_pk_fma_f32 v[36:37], v[32:33], v[32:33], v[36:37]
	v_mul_f32_e32 v38, v23, v23
	v_mul_f32_e32 v40, v21, v21
	v_pk_add_f32 v[36:37], v[36:37], v[36:37] op_sel:[0,1] op_sel_hi:[1,0]
	v_pk_fma_f32 v[38:39], v[22:23], v[22:23], v[38:39] op_sel_hi:[1,1,0]
	v_pk_fma_f32 v[40:41], v[20:21], v[20:21], v[40:41] op_sel_hi:[1,1,0]
	v_pk_mul_f32 v[42:43], v[18:19], v[18:19]
	v_pk_mul_f32 v[44:45], v[16:17], v[16:17]
	v_pk_add_f32 v[26:27], v[26:27], v[34:35]
	v_mov_b32_e32 v37, v43
	v_mov_b32_e32 v27, v42
	v_mov_b32_e32 v39, v44
	v_mov_b32_e32 v41, v45
	v_pk_add_f32 v[26:27], v[26:27], v[36:37]
	v_pk_add_f32 v[34:35], v[38:39], v[40:41]
	s_nop 0
	v_pk_add_f32 v[26:27], v[26:27], v[34:35]
	v_and_b32_e32 v34, 64, v251
	v_add_f32_e32 v26, v26, v27
	v_add_u32_e32 v34, 64, v34
	s_nop 1
	v_mov_b32_e32 v27, v26
	s_nop 1
	v_permlane16_swap_b32_e32 v26, v27
	s_waitcnt lgkmcnt(0)
	v_add_f32_e32 v26, v26, v27
	s_nop 1
	v_mov_b32_e32 v27, v26
	s_nop 1
	v_permlane32_swap_b32_e32 v26, v27
	s_andn2_b64 vcc, exec, s[54:55]
	s_waitcnt lgkmcnt(0)
	v_add_f32_e32 v26, v26, v27
	v_fmamk_f32 v26, v26, 0x3c800000, v249
	v_rsq_f32_e32 v34, v26
	v_mov_b32_e32 v26, v32
	v_mov_b32_e32 v27, v24
	v_mov_b32_e32 v24, v33
	v_pk_mul_f32 v[30:31], v[30:31], v[34:35] op_sel_hi:[1,0]
	v_pk_mul_f32 v[28:29], v[28:29], v[34:35] op_sel_hi:[1,0]
	v_pk_mul_f32 v[26:27], v[26:27], v[34:35] op_sel_hi:[1,0]
	v_pk_mul_f32 v[24:25], v[24:25], v[34:35] op_sel_hi:[1,0]
	v_pk_mul_f32 v[22:23], v[22:23], v[34:35] op_sel_hi:[1,0]
	v_pk_mul_f32 v[20:21], v[20:21], v[34:35] op_sel_hi:[1,0]
	v_pk_mul_f32 v[18:19], v[18:19], v[34:35] op_sel_hi:[1,0]
	v_pk_mul_f32 v[16:17], v[16:17], v[34:35] op_sel_hi:[1,0]
	v_pk_mul_f32 v[28:29], v[70:71], v[28:29]
	v_pk_mul_f32 v[30:31], v[68:69], v[30:31]
	v_pk_mul_f32 v[24:25], v[66:67], v[24:25]
	v_pk_mul_f32 v[26:27], v[64:65], v[26:27]
	v_pk_mul_f32 v[20:21], v[78:79], v[20:21]
	v_pk_mul_f32 v[22:23], v[76:77], v[22:23]
	v_pk_mul_f32 v[16:17], v[74:75], v[16:17]
	v_pk_mul_f32 v[18:19], v[72:73], v[18:19]
	s_cbranch_vccnz .LBB0_425
	v_pk_add_f32 v[94:95], v[94:95], v[28:29]
	v_pk_add_f32 v[92:93], v[92:93], v[30:31]
	v_pk_add_f32 v[90:91], v[90:91], v[24:25]
	v_pk_add_f32 v[88:89], v[88:89], v[26:27]
	v_pk_add_f32 v[86:87], v[86:87], v[20:21]
	v_pk_add_f32 v[84:85], v[84:85], v[22:23]
	v_pk_add_f32 v[82:83], v[82:83], v[16:17]
	v_pk_add_f32 v[80:81], v[80:81], v[18:19]
	s_branch .LBB0_425

; __device__ __forceinline__ float sigmoidf_fast(float x) { return fast_rcp(1.0f + fast_exp2(-x * LOG2E)); }
; __device__ __forceinline__ u32x4 pack8(const f32x4& a, const f32x4& b) { u32x4 w; w.x = pk_bf16(a[0], a[1]); w.y = pk_bf16(a[2], a[3]); w.z = pk_bf16(b[0], b[1]); w.w = pk_bf16(b[2], b[3]); return w; }
;     __device__ __forceinline__ void operator()(const pg8::i32x4 (&acc)[2][2][4][2], const pg8::Unit& u, int wr, int wc, int fr, int fq) const {
;     ...
;             for (int m = 0; m < 4; ++m) {
;                 const int row = u.pm * 256 + ai * 128 + wr * 64 + m * 16 + fr;
;                 const float rs = sq[ai][m];
;                 f32x4 v[2][2];
; #pragma unroll
;                 for (int bj = 0; bj < 2; ++bj)
; #pragma unroll
;                     for (int n = 0; n < 2; ++n)
; #pragma unroll
;                         for (int j = 0; j < 4; ++j) v[bj][n][j] = (float)acc[ai][bj][m][n][j] * (rs * csc[bj][n][j]);
;                 if (kind == 1 || kind == 2) {
;                     float ss = 0.f;
; #pragma unroll
;                     for (int bj = 0; bj < 2; ++bj)
; #pragma unroll
;                         for (int n = 0; n < 2; ++n) ss += (v[bj][n][0] * v[bj][n][0] + v[bj][n][1] * v[bj][n][1]) + (v[bj][n][2] * v[bj][n][2] + v[bj][n][3] * v[bj][n][3]);
;                     ss += __shfl_xor(ss, 16); ss += __shfl_xor(ss, 32);
;                     const float hr = __builtin_amdgcn_rsqf(ss * (1.0f / HD) + EPS);
; #pragma unroll
;                     for (int bj = 0; bj < 2; ++bj)
; #pragma unroll
;                         for (int n = 0; n < 2; ++n) v[bj][n] = v[bj][n] * hr * gv[bj][n];
;                     if (do_kmean) {
; #pragma unroll
;                         for (int bj = 0; bj < 2; ++bj)
; #pragma unroll
;                             for (int n = 0; n < 2; ++n) cs[bj][n] += v[bj][n];
;                     }
;                 } else if (kind == 3) {
; #pragma unroll
;                     for (int bj = 0; bj < 2; ++bj)
; #pragma unroll
;                         for (int n = 0; n < 2; ++n)
; #pragma unroll
;                             for (int j = 0; j < 4; ++j) v[bj][n][j] = sigmoidf_fast(v[bj][n][j] + gv[bj][n][j]);
;                 }
;                 bf16_t* rowp = dst + (size_t)row * ld + col0;
; #pragma unroll
;                 for (int bj = 0; bj < 2; ++bj) if (!dry) *(u32x4*)(rowp + 32 * bj) = pack8(v[bj][0], v[bj][1]);
.LBB0_425:
	v_mul_lo_u32 v34, s53, v178
	v_mul_lo_u32 v35, s52, v179
	v_mad_u64_u32 v[32:33], s[56:57], s52, v178, 0
	v_add3_u32 v33, v33, v35, v34
	v_cvt_f32_i32_e32 v13, v13
	v_cvt_f32_i32_e32 v12, v12
	v_lshl_add_u64 v[34:35], v[32:33], 1, v[114:115]
	v_cvt_pk_bf16_f32 v33, v24, v25
	v_cvt_pk_bf16_f32 v25, v16, v17
	v_cvt_f32_i32_e32 v17, v15
	v_cvt_f32_i32_e32 v16, v14
	v_pk_mul_f32 v[14:15], v[176:177], v[160:161] op_sel_hi:[0,1]
	v_pk_mul_f32 v[14:15], v[14:15], v[12:13]
	v_pk_mul_f32 v[12:13], v[176:177], v[162:163] op_sel_hi:[0,1]
	v_pk_mul_f32 v[12:13], v[12:13], v[16:17]
	v_cvt_f32_i32_e32 v17, v10
	v_cvt_f32_i32_e32 v16, v8
	v_cvt_f32_i32_e32 v11, v11
	v_cvt_f32_i32_e32 v10, v9
	v_cvt_pk_bf16_f32 v24, v18, v19
	v_pk_mul_f32 v[8:9], v[176:177], v[156:157] op_sel_hi:[0,1]
	v_pk_mul_f32 v[18:19], v[176:177], v[158:159] op_sel_hi:[0,1]
	v_cvt_f32_i32_e32 v5, v5
	v_cvt_f32_i32_e32 v4, v4
	v_pk_mul_f32 v[16:17], v[8:9], v[16:17]
	v_pk_mul_f32 v[8:9], v[18:19], v[10:11]
	v_cvt_f32_i32_e32 v11, v7
	v_cvt_f32_i32_e32 v10, v6
	v_cvt_f32_i32_e32 v1, v1
	v_cvt_f32_i32_e32 v0, v0
	v_cvt_pk_bf16_f32 v30, v30, v31
	v_cvt_pk_bf16_f32 v31, v28, v29
	v_cvt_pk_bf16_f32 v32, v26, v27
	v_cvt_pk_bf16_f32 v22, v22, v23
	v_cvt_pk_bf16_f32 v23, v20, v21
	v_pk_mul_f32 v[6:7], v[176:177], v[152:153] op_sel_hi:[0,1]
	v_cvt_f32_i32_e32 v19, v3
	v_cvt_f32_i32_e32 v18, v2
	flat_store_dwordx4 v[34:35], v[30:33]
	flat_store_dwordx4 v[34:35], v[22:25] offset:64
	v_pk_mul_f32 v[6:7], v[6:7], v[4:5]
	v_pk_mul_f32 v[4:5], v[176:177], v[154:155] op_sel_hi:[0,1]
	v_pk_mul_f32 v[4:5], v[4:5], v[10:11]
	v_pk_mul_f32 v[10:11], v[176:177], v[148:149] op_sel_hi:[0,1]
	v_pk_mul_f32 v[2:3], v[10:11], v[0:1]
	v_pk_mul_f32 v[0:1], v[176:177], v[150:151] op_sel_hi:[0,1]
	s_and_b64 vcc, exec, s[4:5]
	v_pk_mul_f32 v[0:1], v[0:1], v[18:19]
	s_cbranch_vccnz .LBB0_428
	v_mul_f32_e32 v10, v15, v15
	v_mul_f32_e32 v18, v13, v13
	v_pk_mul_f32 v[20:21], v[8:9], v[8:9]
	v_pk_fma_f32 v[10:11], v[14:15], v[14:15], v[10:11] op_sel_hi:[1,1,0]
	v_pk_fma_f32 v[18:19], v[12:13], v[12:13], v[18:19] op_sel_hi:[1,1,0]
	v_pk_fma_f32 v[20:21], v[16:17], v[16:17], v[20:21]
	v_mul_f32_e32 v22, v7, v7
	v_mul_f32_e32 v24, v5, v5
	v_pk_add_f32 v[20:21], v[20:21], v[20:21] op_sel:[0,1] op_sel_hi:[1,0]
	v_pk_fma_f32 v[22:23], v[6:7], v[6:7], v[22:23] op_sel_hi:[1,1,0]
	v_pk_fma_f32 v[24:25], v[4:5], v[4:5], v[24:25] op_sel_hi:[1,1,0]
	v_pk_mul_f32 v[26:27], v[2:3], v[2:3]
	v_pk_mul_f32 v[28:29], v[0:1], v[0:1]
	v_pk_add_f32 v[10:11], v[10:11], v[18:19]
	v_mov_b32_e32 v21, v27
	v_mov_b32_e32 v11, v26
	v_mov_b32_e32 v23, v28
	v_mov_b32_e32 v25, v29
	v_pk_add_f32 v[10:11], v[10:11], v[20:21]
	v_pk_add_f32 v[18:19], v[22:23], v[24:25]
	s_nop 0
	v_pk_add_f32 v[10:11], v[10:11], v[18:19]
	v_and_b32_e32 v18, 64, v251
	v_add_f32_e32 v10, v10, v11
	v_add_u32_e32 v18, 64, v18
	s_nop 1
	v_mov_b32_e32 v11, v10
	s_nop 1
	v_permlane16_swap_b32_e32 v10, v11
	s_waitcnt lgkmcnt(0)
	v_add_f32_e32 v10, v10, v11
	s_nop 1
	v_mov_b32_e32 v11, v10
	s_nop 1
	v_permlane32_swap_b32_e32 v10, v11
	s_andn2_b64 vcc, exec, s[54:55]
	s_waitcnt lgkmcnt(0)
	v_add_f32_e32 v10, v10, v11
	v_fmamk_f32 v10, v10, 0x3c800000, v249
	v_rsq_f32_e32 v18, v10
	v_mov_b32_e32 v10, v16
	v_mov_b32_e32 v11, v8
	v_mov_b32_e32 v8, v17
	v_pk_mul_f32 v[14:15], v[14:15], v[18:19] op_sel_hi:[1,0]
	v_pk_mul_f32 v[12:13], v[12:13], v[18:19] op_sel_hi:[1,0]
	v_pk_mul_f32 v[10:11], v[10:11], v[18:19] op_sel_hi:[1,0]
	v_pk_mul_f32 v[8:9], v[8:9], v[18:19] op_sel_hi:[1,0]
	v_pk_mul_f32 v[6:7], v[6:7], v[18:19] op_sel_hi:[1,0]
	v_pk_mul_f32 v[4:5], v[4:5], v[18:19] op_sel_hi:[1,0]
	v_pk_mul_f32 v[2:3], v[2:3], v[18:19] op_sel_hi:[1,0]
	v_pk_mul_f32 v[0:1], v[0:1], v[18:19] op_sel_hi:[1,0]
	v_pk_mul_f32 v[12:13], v[70:71], v[12:13]
	v_pk_mul_f32 v[14:15], v[68:69], v[14:15]
	v_pk_mul_f32 v[8:9], v[66:67], v[8:9]
	v_pk_mul_f32 v[10:11], v[64:65], v[10:11]
	v_pk_mul_f32 v[4:5], v[78:79], v[4:5]
	v_pk_mul_f32 v[6:7], v[76:77], v[6:7]
	v_pk_mul_f32 v[0:1], v[74:75], v[0:1]
	v_pk_mul_f32 v[2:3], v[72:73], v[2:3]
	s_cbranch_vccnz .LBB0_429
	v_pk_add_f32 v[94:95], v[94:95], v[12:13]
	v_pk_add_f32 v[92:93], v[92:93], v[14:15]
	v_pk_add_f32 v[90:91], v[90:91], v[8:9]
	v_pk_add_f32 v[88:89], v[88:89], v[10:11]
	v_pk_add_f32 v[86:87], v[86:87], v[4:5]
	v_pk_add_f32 v[84:85], v[84:85], v[6:7]
	v_pk_add_f32 v[82:83], v[82:83], v[0:1]
	v_pk_add_f32 v[80:81], v[80:81], v[2:3]
	s_branch .LBB0_429

; __device__ __forceinline__ void softmax_pv2(f32x16& a0, f32x16& a1, f32x16& b0, f32x16& b1, f32x16 (&o)[2], float& mref, float& l, f32x16& cn, bool first, LAS float* wsf, ...
;     float ra = fmaxf(fmaxf(a0[0], a0[1]), a1[0]), rb = fmaxf(fmaxf(a0[2], a0[3]), a1[1]), rc = fmaxf(fmaxf(b0[0], b0[1]), b1[0]), rd = fmaxf(fmaxf(b0[2], b0[3]), b1[1]);
;     ra = fmaxf(fmaxf(ra, a1[2]), a1[3]); rc = fmaxf(fmaxf(rc, b1[2]), b1[3]);
; #pragma unroll
;     for (int r = 4; r < 16; r += 4) { ra = fmaxf(fmaxf(ra, a0[r]), a0[r + 1]); rb = fmaxf(fmaxf(rb, a0[r + 2]), a0[r + 3]); ra = fmaxf(fmaxf(ra, a1[r]), a1[r + 1]); rb = fmaxf(fmaxf(rb, a1[r + 2]), a1[r + 3]);
;                                       rc = fmaxf(fmaxf(rc, b0[r]), b0[r + 1]); rd = fmaxf(fmaxf(rd, b0[r + 2]), b0[r + 3]); rc = fmaxf(fmaxf(rc, b1[r]), b1[r + 1]); rd = fmaxf(fmaxf(rd, b1[r + 2]), b1[r + 3]); }
;     float rm = fmaxf(fmaxf(ra, rb), fmaxf(rc, rd)); rm = fmaxf(rm, __shfl_xor(rm, 32));
;     if (first || __any(rm > SM_THR)) {
;         const float dl = first ? rm : fmaxf(rm, 0.f); mref += dl;
.LBB0_670:
	s_nop 8
	v_max_f32_e32 v142, v97, v97
	v_max_f32_e32 v143, v96, v96
	v_max_f32_e32 v142, v143, v142
	v_max3_f32 v140, v80, v81, v64
	v_max3_f32 v143, v98, v99, v49
	v_max3_f32 v142, v142, v48, v50
	v_max3_f32 v141, v82, v83, v65
	v_max3_f32 v140, v140, v66, v67
	v_max3_f32 v142, v142, v51, v100
	v_max3_f32 v143, v143, v102, v103
	v_max3_f32 v140, v140, v84, v85
	v_max3_f32 v141, v141, v86, v87
	v_max3_f32 v142, v142, v101, v52
	v_max3_f32 v143, v143, v54, v55
	v_max3_f32 v140, v140, v68, v69
	v_max3_f32 v141, v141, v70, v71
	v_max3_f32 v142, v142, v53, v104
	v_max3_f32 v143, v143, v106, v107
	v_max3_f32 v140, v140, v88, v89
	v_max3_f32 v141, v141, v90, v91
	v_max3_f32 v142, v142, v105, v56
	v_max3_f32 v143, v143, v58, v59
	v_max3_f32 v140, v140, v72, v73
	v_max3_f32 v141, v141, v74, v75
	v_max3_f32 v142, v142, v57, v108
	v_max3_f32 v143, v143, v110, v111
	v_max3_f32 v140, v140, v92, v93
	v_max3_f32 v141, v141, v94, v95
	v_max3_f32 v142, v142, v109, v60
	v_max3_f32 v143, v143, v62, v63
	v_max3_f32 v140, v140, v76, v77
	v_max3_f32 v141, v141, v78, v79
	v_max3_f32 v142, v142, v61, v143
	v_max3_f32 v140, v140, v141, v142
	v_mov_b32_e32 v141, v140
	s_nop 1
	v_permlane32_swap_b32_e32 v140, v141
	s_cmp_lg_u32 s84, -2
	s_cselect_b64 s[6:7], -1, 0
	s_cmp_eq_u32 s84, -2
	s_mov_b64 s[8:9], -1
	s_waitcnt lgkmcnt(0)
	v_max_f32_e32 v141, v141, v141
	v_max_f32_e32 v140, v140, v141
	s_cbranch_scc1 .LBB0_673
	v_cmp_lt_f32_e32 vcc, s80, v140
	s_cbranch_vccz .LBB0_677
	v_max_f32_e32 v140, v140, v140
	v_max_f32_e32 v140, 0, v140

; __device__ __forceinline__ void softmax_pv2(f32x16& a0, f32x16& a1, f32x16& b0, f32x16& b1, f32x16 (&o)[2], float& mref, float& l, f32x16& cn, bool first, LAS float* wsf, ...
;     float ra = fmaxf(fmaxf(a0[0], a0[1]), a1[0]), rb = fmaxf(fmaxf(a0[2], a0[3]), a1[1]), rc = fmaxf(fmaxf(b0[0], b0[1]), b1[0]), rd = fmaxf(fmaxf(b0[2], b0[3]), b1[1]);
;     ra = fmaxf(fmaxf(ra, a1[2]), a1[3]); rc = fmaxf(fmaxf(rc, b1[2]), b1[3]);
; #pragma unroll
;     for (int r = 4; r < 16; r += 4) { ra = fmaxf(fmaxf(ra, a0[r]), a0[r + 1]); rb = fmaxf(fmaxf(rb, a0[r + 2]), a0[r + 3]); ra = fmaxf(fmaxf(ra, a1[r]), a1[r + 1]); rb = fmaxf(fmaxf(rb, a1[r + 2]), a1[r + 3]);
;                                       rc = fmaxf(fmaxf(rc, b0[r]), b0[r + 1]); rd = fmaxf(fmaxf(rd, b0[r + 2]), b0[r + 3]); rc = fmaxf(fmaxf(rc, b1[r]), b1[r + 1]); rd = fmaxf(fmaxf(rd, b1[r + 2]), b1[r + 3]); }
;     float rm = fmaxf(fmaxf(ra, rb), fmaxf(rc, rd)); rm = fmaxf(rm, __shfl_xor(rm, 32));
;     if (first || __any(rm > SM_THR)) {
;         const float dl = first ? rm : fmaxf(rm, 0.f); mref += dl;
.LBB0_748:
	s_nop 8
	v_max_f32_e32 v140, v97, v97
	v_max_f32_e32 v141, v96, v96
	v_max_f32_e32 v140, v141, v140
	v_max3_f32 v138, v80, v81, v64
	v_max3_f32 v141, v98, v99, v49
	v_max3_f32 v140, v140, v48, v50
	v_max3_f32 v139, v82, v83, v65
	v_max3_f32 v138, v138, v66, v67
	v_max3_f32 v140, v140, v51, v100
	v_max3_f32 v141, v141, v102, v103
	v_max3_f32 v138, v138, v84, v85
	v_max3_f32 v139, v139, v86, v87
	v_max3_f32 v140, v140, v101, v52
	v_max3_f32 v141, v141, v54, v55
	v_max3_f32 v138, v138, v68, v69
	v_max3_f32 v139, v139, v70, v71
	v_max3_f32 v140, v140, v53, v104
	v_max3_f32 v141, v141, v106, v107
	v_max3_f32 v138, v138, v88, v89
	v_max3_f32 v139, v139, v90, v91
	v_max3_f32 v140, v140, v105, v56
	v_max3_f32 v141, v141, v58, v59
	v_max3_f32 v138, v138, v72, v73
	v_max3_f32 v139, v139, v74, v75
	v_max3_f32 v140, v140, v57, v108
	v_max3_f32 v141, v141, v110, v111
	v_max3_f32 v138, v138, v92, v93
	v_max3_f32 v139, v139, v94, v95
	v_max3_f32 v140, v140, v109, v60
	v_max3_f32 v141, v141, v62, v63
	v_max3_f32 v138, v138, v76, v77
	v_max3_f32 v139, v139, v78, v79
	v_max3_f32 v140, v140, v61, v141
	v_max3_f32 v138, v138, v139, v140
	v_mov_b32_e32 v139, v138
	s_nop 1
	v_permlane32_swap_b32_e32 v138, v139
	s_cmp_lg_u32 s72, -2
	s_cselect_b64 s[6:7], -1, 0
	s_cmp_eq_u32 s72, -2
	s_mov_b64 s[8:9], -1
	s_waitcnt lgkmcnt(0)
	v_max_f32_e32 v139, v139, v139
	v_max_f32_e32 v138, v138, v139
	s_cbranch_scc1 .LBB0_751
	v_cmp_lt_f32_e32 vcc, s80, v138
	s_cbranch_vccz .LBB0_755
	v_max_f32_e32 v138, v138, v138
	v_max_f32_e32 v138, 0, v138

; __device__ __forceinline__ int fresh_tid(int wave) { return wave * 64 + fresh_lane(); }
; __device__ __forceinline__ unsigned xb_ld(unsigned* p)              { return __hip_atomic_load(p, __ATOMIC_RELAXED, __HIP_MEMORY_SCOPE_AGENT); }
; __device__ __forceinline__ unsigned xb_add(unsigned* p, unsigned v) { return __hip_atomic_fetch_add(p, v, __ATOMIC_RELAXED, __HIP_MEMORY_SCOPE_AGENT); }
; __device__ __forceinline__ unsigned xb_xcc_id() { return (unsigned)__builtin_amdgcn_s_getreg((3 << 11) | 20) & 0xFu; }
; #define XB_SPIN(cond, bar) do { unsigned _sp = 0; while (cond) { __builtin_amdgcn_s_sleep(1); \
;     if ((++_sp & 255u) == 0u) { if (xb_ld(&(bar)[XB_TMO])) break; if (_sp > XB_SPIN_CAP) { atomicAdd(&(bar)[XB_TMO], 1u); break; } } } } while (0)
; __device__ __forceinline__ void xcd_barrier(const XcdBarrier& b) {
;     asm volatile("s_waitcnt vmcnt(0)" ::: "memory");
;     __syncthreads();
;     if (fresh_tid(b.wave) == 0) {
;         unsigned* bar = b.bar; asm volatile("" : "+s"(bar));
;         __builtin_amdgcn_s_waitcnt(0);
;         const unsigned bx = xb_xcc_id();
;         unsigned nloc = b.st[0], nx = b.st[1];
;         if (nloc == 0u) { xcd_barrier_complete(bar, bx, nloc, nx); b.st[0] = nloc; b.st[1] = nx; }
;         const unsigned old = xb_add(&bar[XB_XSUB(bx)], 1u);
;         const unsigned gen = old / nloc;
;         if (old + 1u == (gen + 1u) * nloc) {
;             __builtin_amdgcn_fence(__ATOMIC_RELEASE, "agent");
;             asm volatile("s_waitcnt vmcnt(0)" ::: "memory");
;             const unsigned og = xb_add(&bar[XB_TOP], 1u);
;             const unsigned tg = og / nx;
;             if (og + 1u == (tg + 1u) * nx) xb_add(&bar[XB_TOPGEN], 1u);
;             else XB_SPIN(xb_ld(&bar[XB_TOPGEN]) == tg, bar);
;             __builtin_amdgcn_fence(__ATOMIC_ACQUIRE, "agent");
;             xb_add(&bar[XB_XGEN(bx)], 1u);
;             asm volatile("s_waitcnt vmcnt(0)" ::: "memory");
;         } else {
;             XB_SPIN(xb_ld(&bar[XB_XGEN(bx)]) == gen, bar);
;             __builtin_amdgcn_fence(__ATOMIC_ACQUIRE, "agent");
;             asm volatile("s_waitcnt vmcnt(0)" ::: "memory");
;         }
.LBB0_1023:
	s_mov_b32 s0, s93
	s_waitcnt vmcnt(0)
	s_waitcnt lgkmcnt(0)
	s_barrier
	s_nop 0
	v_mbcnt_lo_u32_b32 v0, -1, s0
	v_mbcnt_hi_u32_b32 v0, -1, v0
	v_readlane_b32 s0, v254, 17
	s_nop 1
	v_cmp_eq_u32_e32 vcc, s0, v0
	s_and_saveexec_b64 s[0:1], vcc
	s_cbranch_execz .LBB0_1067
	s_bitcmp1_b32 s100, 0
	s_cbranch_scc0 .Llb_mg_glob
	v_readlane_b32 s2, v253, 53
	v_readlane_b32 s3, v253, 54
	v_readlane_b32 s4, v253, 0
	v_mov_b32_e32 v1, 1
	s_and_b32 s4, s4, 7
	s_lshl_b32 s4, s4, 8
	s_addk_i32 s4, 0x480
	v_mov_b32_e32 v0, s4
	s_waitcnt vmcnt(0) lgkmcnt(0)
	global_atomic_add v0, v1, s[2:3]
	s_add_i32 s101, s101, 32
	s_mov_b32 s5, 0
	v_mov_b32_e32 v2, s101

; __device__ __forceinline__ int fresh_tid(int wave) { return wave * 64 + fresh_lane(); }
; __device__ __forceinline__ unsigned xb_add(unsigned* p, unsigned v) { return __hip_atomic_fetch_add(p, v, __ATOMIC_RELAXED, __HIP_MEMORY_SCOPE_AGENT); }
; __device__ __forceinline__ unsigned xb_xcc_id() { return (unsigned)__builtin_amdgcn_s_getreg((3 << 11) | 20) & 0xFu; }
; __device__ __forceinline__ void xcd_barrier(const XcdBarrier& b) {
;     asm volatile("s_waitcnt vmcnt(0)" ::: "memory");
;     __syncthreads();
;     if (fresh_tid(b.wave) == 0) {
;         unsigned* bar = b.bar; asm volatile("" : "+s"(bar));
;         __builtin_amdgcn_s_waitcnt(0);
;         const unsigned bx = xb_xcc_id();
;         unsigned nloc = b.st[0], nx = b.st[1];
;         if (nloc == 0u) { xcd_barrier_complete(bar, bx, nloc, nx); b.st[0] = nloc; b.st[1] = nx; }
;         const unsigned old = xb_add(&bar[XB_XSUB(bx)], 1u);
;         const unsigned gen = old / nloc;
;         if (old + 1u == (gen + 1u) * nloc) {
.LBB0_1237:
	s_mov_b32 s0, s93
	s_waitcnt lgkmcnt(0)
	s_barrier
	s_waitcnt vmcnt(0)
	s_barrier
	s_nop 0
	v_mbcnt_lo_u32_b32 v0, -1, s0
	v_mbcnt_hi_u32_b32 v0, -1, v0
	v_readlane_b32 s0, v254, 17
	s_nop 1
	v_cmp_eq_u32_e32 vcc, s0, v0
	s_and_saveexec_b64 s[0:1], vcc
	s_cbranch_execz .LBB0_1281
	s_bitcmp1_b32 s100, 0
	s_cbranch_scc0 .Llb_x2_glob
	v_readlane_b32 s2, v253, 53
	v_readlane_b32 s3, v253, 54
	v_readlane_b32 s4, v253, 0
	v_mov_b32_e32 v1, 1
	s_and_b32 s4, s4, 7
	s_lshl_b32 s4, s4, 8
	s_addk_i32 s4, 0x480
	v_mov_b32_e32 v0, s4
	s_waitcnt vmcnt(0) lgkmcnt(0)
	global_atomic_add v0, v1, s[2:3]
	s_add_i32 s101, s101, 32
	s_mov_b32 s5, 0
	v_mov_b32_e32 v2, s101

; __device__ __forceinline__ int fresh_tid(int wave) { return wave * 64 + fresh_lane(); }
; __device__ __forceinline__ unsigned xb_ld(unsigned* p)              { return __hip_atomic_load(p, __ATOMIC_RELAXED, __HIP_MEMORY_SCOPE_AGENT); }
; __device__ __forceinline__ unsigned xb_add(unsigned* p, unsigned v) { return __hip_atomic_fetch_add(p, v, __ATOMIC_RELAXED, __HIP_MEMORY_SCOPE_AGENT); }
; __device__ __forceinline__ unsigned xb_xcc_id() { return (unsigned)__builtin_amdgcn_s_getreg((3 << 11) | 20) & 0xFu; }
; #define XB_SPIN(cond, bar) do { unsigned _sp = 0; while (cond) { __builtin_amdgcn_s_sleep(1); \
;     if ((++_sp & 255u) == 0u) { if (xb_ld(&(bar)[XB_TMO])) break; if (_sp > XB_SPIN_CAP) { atomicAdd(&(bar)[XB_TMO], 1u); break; } } } } while (0)
; __device__ __forceinline__ void xcd_barrier(const XcdBarrier& b) {
;     asm volatile("s_waitcnt vmcnt(0)" ::: "memory");
;     __syncthreads();
;     if (fresh_tid(b.wave) == 0) {
;         unsigned* bar = b.bar; asm volatile("" : "+s"(bar));
;         __builtin_amdgcn_s_waitcnt(0);
;         const unsigned bx = xb_xcc_id();
;         unsigned nloc = b.st[0], nx = b.st[1];
;         if (nloc == 0u) { xcd_barrier_complete(bar, bx, nloc, nx); b.st[0] = nloc; b.st[1] = nx; }
;         const unsigned old = xb_add(&bar[XB_XSUB(bx)], 1u);
;         const unsigned gen = old / nloc;
;         if (old + 1u == (gen + 1u) * nloc) {
;             __builtin_amdgcn_fence(__ATOMIC_RELEASE, "agent");
;             asm volatile("s_waitcnt vmcnt(0)" ::: "memory");
;             const unsigned og = xb_add(&bar[XB_TOP], 1u);
;             const unsigned tg = og / nx;
;             if (og + 1u == (tg + 1u) * nx) xb_add(&bar[XB_TOPGEN], 1u);
;             else XB_SPIN(xb_ld(&bar[XB_TOPGEN]) == tg, bar);
;             __builtin_amdgcn_fence(__ATOMIC_ACQUIRE, "agent");
;             xb_add(&bar[XB_XGEN(bx)], 1u);
;             asm volatile("s_waitcnt vmcnt(0)" ::: "memory");
;         } else {
;             XB_SPIN(xb_ld(&bar[XB_XGEN(bx)]) == gen, bar);
;             __builtin_amdgcn_fence(__ATOMIC_ACQUIRE, "agent");
;             asm volatile("s_waitcnt vmcnt(0)" ::: "memory");
;         }
.LBB0_1774:
	s_mov_b32 s0, s93
	s_waitcnt vmcnt(0)
	s_waitcnt lgkmcnt(0)
	s_barrier
	s_nop 0
	v_mbcnt_lo_u32_b32 v0, -1, s0
	v_mbcnt_hi_u32_b32 v0, -1, v0
	v_readlane_b32 s0, v254, 17
	s_nop 1
	v_cmp_eq_u32_e32 vcc, s0, v0
	s_and_saveexec_b64 s[30:31], vcc
	s_cbranch_execz .LBB0_1818
	s_bitcmp1_b32 s100, 0
	s_cbranch_scc0 .Llb_f1_glob
	v_readlane_b32 s34, v253, 53
	v_readlane_b32 s35, v253, 54
	v_readlane_b32 s0, v253, 0
	v_mov_b32_e32 v1, 1
	s_and_b32 s0, s0, 7
	s_lshl_b32 s0, s0, 8
	s_addk_i32 s0, 0x480
	v_mov_b32_e32 v0, s0
	s_waitcnt vmcnt(0) lgkmcnt(0)
	global_atomic_add v0, v1, s[34:35]
	s_add_i32 s101, s101, 32
	s_mov_b32 s1, 0
	v_mov_b32_e32 v2, s101
